# combined: barrier change + per-unit VMEM drains dropped (K-loop preheaders, scalar load of next expert id) + latent-attention unit-boundary waits relaxed + s_setprio removed from GEMM K-loops
# speedup vs baseline: 1.0089x; 1.0034x over previous
; template <class Epi, class Sched, bool ALIGN_EPI = false, bool SP2 = false, bool F8 = false, bool I8 = false, bool PF = false>
; __device__ __forceinline__ void gemm_phase(PG8_LAS unsigned char* lds, const Gemm g, const Sched& S, const Epi& E, const int wave_) {
;     ...
;         const bool has_next = S.next(ui + 1, nxt);
;         const char* nA = has_next ? (const char*)g.A + (size_t)nxt.pm * tstep : cA; const char* nB = has_next ? (const char*)g.Bt + (size_t)nxt.pb * tstep : cB;
;         for (int t = 0; t < nt; t += 2) {
;             const bool last = (t == nt - 2);
;             const char* a1 = cA + (size_t)(t + 1) * kstep;
;             const char* a2 = last ? nA : cA + (size_t)(t + 2) * kstep; const char* b2 = last ? nB : cB + (size_t)(t + 2) * kstep;
;     ...
; #pragma unroll
;         for (int a = 0; a < 2; ++a)
; #pragma unroll
;             for (int b = 0; b < 2; ++b)
; #pragma unroll
;                 for (int m = 0; m < 4; ++m)
; #pragma unroll
;                     for (int n = 0; n < 2; ++n) acc[a][b][m][n] = (f32x4){0.f, 0.f, 0.f, 0.f};
;         cur = nxt; cA = nA; cB = nB; ++ui;
.LBB0_241:
	s_ashr_i32 s41, s40, 31
	s_lshl_b64 s[44:45], s[40:41], 18
	s_add_u32 s44, s58, s44
	s_addc_u32 s45, s59, s45
	s_and_b64 s[46:47], s[42:43], exec
	s_cselect_b32 s1, s45, s49
	s_cselect_b32 s5, s44, s48
	s_ashr_i32 s39, s38, 31
	s_lshl_b64 s[46:47], s[38:39], 18
	s_add_u32 s46, s29, s46
	s_addc_u32 s47, s31, s47
	s_and_b64 s[52:53], s[42:43], exec
	s_cselect_b32 s39, s47, s51
	s_cselect_b32 s41, s46, s50
	s_add_u32 s48, s48, 0x20080
	s_addc_u32 s49, s49, 0
	s_add_u32 s75, s50, 0x100
	v_mov_b32_e32 v0, 0
	s_addc_u32 s78, s51, 0
	s_mov_b32 s79, -2
	v_mov_b32_e32 v1, v0
	v_mov_b32_e32 v2, v0
	v_mov_b32_e32 v3, v0
	v_mov_b32_e32 v4, v0
	v_mov_b32_e32 v5, v0
	v_mov_b32_e32 v6, v0
	v_mov_b32_e32 v7, v0
	v_mov_b32_e32 v16, v0
	v_mov_b32_e32 v17, v0
	v_mov_b32_e32 v18, v0
	v_mov_b32_e32 v19, v0
	v_mov_b32_e32 v20, v0
	v_mov_b32_e32 v21, v0
	v_mov_b32_e32 v22, v0
	v_mov_b32_e32 v23, v0
	v_mov_b32_e32 v32, v0
	v_mov_b32_e32 v33, v0
	v_mov_b32_e32 v34, v0
	v_mov_b32_e32 v35, v0
	v_mov_b32_e32 v36, v0
	v_mov_b32_e32 v37, v0
	v_mov_b32_e32 v38, v0
	v_mov_b32_e32 v39, v0
	v_mov_b32_e32 v48, v0
	v_mov_b32_e32 v49, v0
	v_mov_b32_e32 v50, v0
	v_mov_b32_e32 v51, v0
	v_mov_b32_e32 v52, v0
	v_mov_b32_e32 v53, v0
	v_mov_b32_e32 v54, v0
	v_mov_b32_e32 v55, v0
	v_mov_b32_e32 v8, v0
	v_mov_b32_e32 v9, v0
	v_mov_b32_e32 v10, v0
	v_mov_b32_e32 v11, v0
	v_mov_b32_e32 v12, v0
	v_mov_b32_e32 v13, v0
	v_mov_b32_e32 v14, v0
	v_mov_b32_e32 v15, v0
	v_mov_b32_e32 v24, v0
	v_mov_b32_e32 v25, v0
	v_mov_b32_e32 v26, v0
	v_mov_b32_e32 v27, v0
	v_mov_b32_e32 v28, v0
	v_mov_b32_e32 v29, v0
	v_mov_b32_e32 v30, v0
	v_mov_b32_e32 v31, v0
	v_mov_b32_e32 v40, v0
	v_mov_b32_e32 v41, v0
	v_mov_b32_e32 v42, v0
	v_mov_b32_e32 v43, v0
	v_mov_b32_e32 v44, v0
	v_mov_b32_e32 v45, v0
	v_mov_b32_e32 v46, v0
	v_mov_b32_e32 v47, v0
	v_mov_b32_e32 v56, v0
	v_mov_b32_e32 v57, v0
	v_mov_b32_e32 v58, v0
	v_mov_b32_e32 v59, v0
	v_mov_b32_e32 v60, v0
	v_mov_b32_e32 v61, v0
	v_mov_b32_e32 v62, v0
	v_mov_b32_e32 v63, v0
	v_mov_b32_e32 v64, v0
	v_mov_b32_e32 v65, v0
	v_mov_b32_e32 v66, v0
	v_mov_b32_e32 v67, v0
	v_mov_b32_e32 v68, v0
	v_mov_b32_e32 v69, v0
	v_mov_b32_e32 v70, v0
	v_mov_b32_e32 v71, v0
	v_mov_b32_e32 v80, v0
	v_mov_b32_e32 v81, v0
	v_mov_b32_e32 v82, v0
	v_mov_b32_e32 v83, v0
	v_mov_b32_e32 v84, v0
	v_mov_b32_e32 v85, v0
	v_mov_b32_e32 v86, v0
	v_mov_b32_e32 v87, v0
	v_mov_b32_e32 v96, v0
	v_mov_b32_e32 v97, v0
	v_mov_b32_e32 v98, v0
	v_mov_b32_e32 v99, v0
	v_mov_b32_e32 v100, v0
	v_mov_b32_e32 v101, v0
	v_mov_b32_e32 v102, v0
	v_mov_b32_e32 v103, v0
	v_mov_b32_e32 v112, v0
	v_mov_b32_e32 v113, v0
	v_mov_b32_e32 v114, v0
	v_mov_b32_e32 v115, v0
	v_mov_b32_e32 v116, v0
	v_mov_b32_e32 v117, v0
	v_mov_b32_e32 v118, v0
	v_mov_b32_e32 v119, v0
	v_mov_b32_e32 v72, v0
	v_mov_b32_e32 v73, v0
	v_mov_b32_e32 v74, v0
	v_mov_b32_e32 v75, v0
	v_mov_b32_e32 v76, v0
	v_mov_b32_e32 v77, v0
	v_mov_b32_e32 v78, v0
	v_mov_b32_e32 v79, v0
	v_mov_b32_e32 v88, v0
	v_mov_b32_e32 v89, v0
	v_mov_b32_e32 v90, v0
	v_mov_b32_e32 v91, v0
	v_mov_b32_e32 v92, v0
	v_mov_b32_e32 v93, v0
	v_mov_b32_e32 v94, v0
	v_mov_b32_e32 v95, v0
	v_mov_b32_e32 v104, v0
	v_mov_b32_e32 v105, v0
	v_mov_b32_e32 v106, v0
	v_mov_b32_e32 v107, v0
	v_mov_b32_e32 v108, v0
	v_mov_b32_e32 v109, v0
	v_mov_b32_e32 v110, v0
	v_mov_b32_e32 v111, v0
	v_mov_b32_e32 v120, v0
	v_mov_b32_e32 v121, v0
	v_mov_b32_e32 v122, v0
	v_mov_b32_e32 v123, v0
	v_mov_b32_e32 v124, v0
	v_mov_b32_e32 v125, v0
	v_mov_b32_e32 v126, v0
	v_mov_b32_e32 v127, v0

; template <class Epi, class Sched, bool ALIGN_EPI = false, bool SP2 = false, bool F8 = false, bool I8 = false, bool PF = false>
; __device__ __forceinline__ void gemm_phase(PG8_LAS unsigned char* lds, const Gemm g, const Sched& S, const Epi& E, const int wave_) {
;     ...
;         const bool has_next = S.next(ui + 1, nxt);
;         const char* nA = has_next ? (const char*)g.A + (size_t)nxt.pm * tstep : cA; const char* nB = has_next ? (const char*)g.Bt + (size_t)nxt.pb * tstep : cB;
;         for (int t = 0; t < nt; t += 2) {
;             const bool last = (t == nt - 2);
;             const char* a1 = cA + (size_t)(t + 1) * kstep;
;             const char* a2 = last ? nA : cA + (size_t)(t + 2) * kstep; const char* b2 = last ? nB : cB + (size_t)(t + 2) * kstep;
;     ...
; #pragma unroll
;         for (int a = 0; a < 2; ++a)
; #pragma unroll
;             for (int b = 0; b < 2; ++b)
; #pragma unroll
;                 for (int m = 0; m < 4; ++m)
; #pragma unroll
;                     for (int n = 0; n < 2; ++n) acc[a][b][m][n] = (f32x4){0.f, 0.f, 0.f, 0.f};
;         cur = nxt; cA = nA; cB = nB; ++ui;
.LBB0_452:
	s_ashr_i32 s13, s12, 31
	s_lshl_b64 s[16:17], s[12:13], 19
	s_add_u32 s16, s26, s16
	s_addc_u32 s17, s27, s17
	s_and_b64 s[18:19], s[14:15], exec
	s_cselect_b32 s13, s17, s23
	s_cselect_b32 s52, s16, s22
	s_ashr_i32 s11, s10, 31
	s_lshl_b64 s[18:19], s[10:11], 19
	s_add_u32 s18, s34, s18
	s_addc_u32 s19, s35, s19
	s_and_b64 s[30:31], s[14:15], exec
	s_cselect_b32 s11, s19, s29
	s_cselect_b32 s53, s18, s28
	s_add_u32 s22, s22, 0x40080
	s_addc_u32 s23, s23, 0
	s_add_u32 s54, s28, 0x100
	v_mov_b32_e32 v0, 0
	s_addc_u32 s55, s29, 0
	s_mov_b32 s62, -2
	v_mov_b32_e32 v1, v0
	v_mov_b32_e32 v2, v0
	v_mov_b32_e32 v3, v0
	v_mov_b32_e32 v4, v0
	v_mov_b32_e32 v5, v0
	v_mov_b32_e32 v6, v0
	v_mov_b32_e32 v7, v0
	v_mov_b32_e32 v12, v0
	v_mov_b32_e32 v13, v0
	v_mov_b32_e32 v14, v0
	v_mov_b32_e32 v15, v0
	v_mov_b32_e32 v20, v0
	v_mov_b32_e32 v21, v0
	v_mov_b32_e32 v22, v0
	v_mov_b32_e32 v23, v0
	v_mov_b32_e32 v28, v0
	v_mov_b32_e32 v29, v0
	v_mov_b32_e32 v30, v0
	v_mov_b32_e32 v31, v0
	v_mov_b32_e32 v36, v0
	v_mov_b32_e32 v37, v0
	v_mov_b32_e32 v38, v0
	v_mov_b32_e32 v39, v0
	v_mov_b32_e32 v44, v0
	v_mov_b32_e32 v45, v0
	v_mov_b32_e32 v46, v0
	v_mov_b32_e32 v47, v0
	v_mov_b32_e32 v52, v0
	v_mov_b32_e32 v53, v0
	v_mov_b32_e32 v54, v0
	v_mov_b32_e32 v55, v0
	v_mov_b32_e32 v8, v0
	v_mov_b32_e32 v9, v0
	v_mov_b32_e32 v10, v0
	v_mov_b32_e32 v11, v0
	v_mov_b32_e32 v16, v0
	v_mov_b32_e32 v17, v0
	v_mov_b32_e32 v18, v0
	v_mov_b32_e32 v19, v0
	v_mov_b32_e32 v24, v0
	v_mov_b32_e32 v25, v0
	v_mov_b32_e32 v26, v0
	v_mov_b32_e32 v27, v0
	v_mov_b32_e32 v32, v0
	v_mov_b32_e32 v33, v0
	v_mov_b32_e32 v34, v0
	v_mov_b32_e32 v35, v0
	v_mov_b32_e32 v40, v0
	v_mov_b32_e32 v41, v0
	v_mov_b32_e32 v42, v0
	v_mov_b32_e32 v43, v0
	v_mov_b32_e32 v48, v0
	v_mov_b32_e32 v49, v0
	v_mov_b32_e32 v50, v0
	v_mov_b32_e32 v51, v0
	v_mov_b32_e32 v56, v0
	v_mov_b32_e32 v57, v0
	v_mov_b32_e32 v58, v0
	v_mov_b32_e32 v59, v0
	v_mov_b32_e32 v60, v0
	v_mov_b32_e32 v61, v0
	v_mov_b32_e32 v62, v0
	v_mov_b32_e32 v63, v0
	v_mov_b32_e32 v64, v0
	v_mov_b32_e32 v65, v0
	v_mov_b32_e32 v66, v0
	v_mov_b32_e32 v67, v0
	v_mov_b32_e32 v68, v0
	v_mov_b32_e32 v69, v0
	v_mov_b32_e32 v70, v0
	v_mov_b32_e32 v71, v0
	v_mov_b32_e32 v76, v0
	v_mov_b32_e32 v77, v0
	v_mov_b32_e32 v78, v0
	v_mov_b32_e32 v79, v0
	v_mov_b32_e32 v84, v0
	v_mov_b32_e32 v85, v0
	v_mov_b32_e32 v86, v0
	v_mov_b32_e32 v87, v0
	v_mov_b32_e32 v92, v0
	v_mov_b32_e32 v93, v0
	v_mov_b32_e32 v94, v0
	v_mov_b32_e32 v95, v0
	v_mov_b32_e32 v100, v0
	v_mov_b32_e32 v101, v0
	v_mov_b32_e32 v102, v0
	v_mov_b32_e32 v103, v0
	v_mov_b32_e32 v104, v0
	v_mov_b32_e32 v105, v0
	v_mov_b32_e32 v106, v0
	v_mov_b32_e32 v107, v0
	v_mov_b32_e32 v108, v0
	v_mov_b32_e32 v109, v0
	v_mov_b32_e32 v110, v0
	v_mov_b32_e32 v111, v0
	v_mov_b32_e32 v72, v0
	v_mov_b32_e32 v73, v0
	v_mov_b32_e32 v74, v0
	v_mov_b32_e32 v75, v0
	v_mov_b32_e32 v80, v0
	v_mov_b32_e32 v81, v0
	v_mov_b32_e32 v82, v0
	v_mov_b32_e32 v83, v0
	v_mov_b32_e32 v88, v0
	v_mov_b32_e32 v89, v0
	v_mov_b32_e32 v90, v0
	v_mov_b32_e32 v91, v0
	v_mov_b32_e32 v96, v0
	v_mov_b32_e32 v97, v0
	v_mov_b32_e32 v98, v0
	v_mov_b32_e32 v99, v0
	v_mov_b32_e32 v112, v0
	v_mov_b32_e32 v113, v0
	v_mov_b32_e32 v114, v0
	v_mov_b32_e32 v115, v0
	v_mov_b32_e32 v116, v0
	v_mov_b32_e32 v117, v0
	v_mov_b32_e32 v118, v0
	v_mov_b32_e32 v119, v0
	v_mov_b32_e32 v120, v0
	v_mov_b32_e32 v121, v0
	v_mov_b32_e32 v122, v0
	v_mov_b32_e32 v123, v0
	v_mov_b32_e32 v124, v0
	v_mov_b32_e32 v125, v0
	v_mov_b32_e32 v126, v0
	v_mov_b32_e32 v127, v0

; template <class Epi, class Sched, bool ALIGN_EPI = false, bool SP2 = false, bool F8 = false, bool I8 = false, bool PF = false>
; __device__ __forceinline__ void gemm_phase(PG8_LAS unsigned char* lds, const Gemm g, const Sched& S, const Epi& E, const int wave_) {
;     ...
;         const bool has_next = S.next(ui + 1, nxt);
;         const char* nA = has_next ? (const char*)g.A + (size_t)nxt.pm * tstep : cA; const char* nB = has_next ? (const char*)g.Bt + (size_t)nxt.pb * tstep : cB;
;         for (int t = 0; t < nt; t += 2) {
;             const bool last = (t == nt - 2);
;             const char* a1 = cA + (size_t)(t + 1) * kstep;
;             const char* a2 = last ? nA : cA + (size_t)(t + 2) * kstep; const char* b2 = last ? nB : cB + (size_t)(t + 2) * kstep;
;     ...
; #pragma unroll
;         for (int a = 0; a < 2; ++a)
; #pragma unroll
;             for (int b = 0; b < 2; ++b)
; #pragma unroll
;                 for (int m = 0; m < 4; ++m)
; #pragma unroll
;                     for (int n = 0; n < 2; ++n) acc[a][b][m][n] = (f32x4){0.f, 0.f, 0.f, 0.f};
;         cur = nxt; cA = nA; cB = nB; ++ui;
.LBB0_590:
	s_ashr_i32 s19, s18, 31
	s_lshl_b64 s[22:23], s[18:19], 18
	s_add_u32 s22, s58, s22
	s_addc_u32 s23, s59, s23
	s_and_b64 s[26:27], s[20:21], exec
	s_cselect_b32 s19, s23, s31
	s_cselect_b32 s56, s22, s30
	s_ashr_i32 s17, s16, 31
	s_lshl_b64 s[26:27], s[16:17], 18
	s_add_u32 s26, s15, s26
	s_addc_u32 s27, s38, s27
	s_and_b64 s[36:37], s[20:21], exec
	s_cselect_b32 s17, s27, s35
	s_cselect_b32 s57, s26, s34
	s_add_u32 s30, s30, 0x20080
	s_addc_u32 s31, s31, 0
	s_add_u32 s62, s34, 0x100
	v_mov_b32_e32 v0, 0
	s_addc_u32 s63, s35, 0
	s_mov_b32 s64, -2
	v_mov_b32_e32 v1, v0
	v_mov_b32_e32 v2, v0
	v_mov_b32_e32 v3, v0
	v_mov_b32_e32 v4, v0
	v_mov_b32_e32 v5, v0
	v_mov_b32_e32 v6, v0
	v_mov_b32_e32 v7, v0
	v_mov_b32_e32 v16, v0
	v_mov_b32_e32 v17, v0
	v_mov_b32_e32 v18, v0
	v_mov_b32_e32 v19, v0
	v_mov_b32_e32 v20, v0
	v_mov_b32_e32 v21, v0
	v_mov_b32_e32 v22, v0
	v_mov_b32_e32 v23, v0
	v_mov_b32_e32 v32, v0
	v_mov_b32_e32 v33, v0
	v_mov_b32_e32 v34, v0
	v_mov_b32_e32 v35, v0
	v_mov_b32_e32 v36, v0
	v_mov_b32_e32 v37, v0
	v_mov_b32_e32 v38, v0
	v_mov_b32_e32 v39, v0
	v_mov_b32_e32 v48, v0
	v_mov_b32_e32 v49, v0
	v_mov_b32_e32 v50, v0
	v_mov_b32_e32 v51, v0
	v_mov_b32_e32 v52, v0
	v_mov_b32_e32 v53, v0
	v_mov_b32_e32 v54, v0
	v_mov_b32_e32 v55, v0
	v_mov_b32_e32 v8, v0
	v_mov_b32_e32 v9, v0
	v_mov_b32_e32 v10, v0
	v_mov_b32_e32 v11, v0
	v_mov_b32_e32 v12, v0
	v_mov_b32_e32 v13, v0
	v_mov_b32_e32 v14, v0
	v_mov_b32_e32 v15, v0
	v_mov_b32_e32 v24, v0
	v_mov_b32_e32 v25, v0
	v_mov_b32_e32 v26, v0
	v_mov_b32_e32 v27, v0
	v_mov_b32_e32 v28, v0
	v_mov_b32_e32 v29, v0
	v_mov_b32_e32 v30, v0
	v_mov_b32_e32 v31, v0
	v_mov_b32_e32 v40, v0
	v_mov_b32_e32 v41, v0
	v_mov_b32_e32 v42, v0
	v_mov_b32_e32 v43, v0
	v_mov_b32_e32 v44, v0
	v_mov_b32_e32 v45, v0
	v_mov_b32_e32 v46, v0
	v_mov_b32_e32 v47, v0
	v_mov_b32_e32 v56, v0
	v_mov_b32_e32 v57, v0
	v_mov_b32_e32 v58, v0
	v_mov_b32_e32 v59, v0
	v_mov_b32_e32 v60, v0
	v_mov_b32_e32 v61, v0
	v_mov_b32_e32 v62, v0
	v_mov_b32_e32 v63, v0
	v_mov_b32_e32 v64, v0
	v_mov_b32_e32 v65, v0
	v_mov_b32_e32 v66, v0
	v_mov_b32_e32 v67, v0
	v_mov_b32_e32 v68, v0
	v_mov_b32_e32 v69, v0
	v_mov_b32_e32 v70, v0
	v_mov_b32_e32 v71, v0
	v_mov_b32_e32 v80, v0
	v_mov_b32_e32 v81, v0
	v_mov_b32_e32 v82, v0
	v_mov_b32_e32 v83, v0
	v_mov_b32_e32 v84, v0
	v_mov_b32_e32 v85, v0
	v_mov_b32_e32 v86, v0
	v_mov_b32_e32 v87, v0
	v_mov_b32_e32 v96, v0
	v_mov_b32_e32 v97, v0
	v_mov_b32_e32 v98, v0
	v_mov_b32_e32 v99, v0
	v_mov_b32_e32 v100, v0
	v_mov_b32_e32 v101, v0
	v_mov_b32_e32 v102, v0
	v_mov_b32_e32 v103, v0
	v_mov_b32_e32 v112, v0
	v_mov_b32_e32 v113, v0
	v_mov_b32_e32 v114, v0
	v_mov_b32_e32 v115, v0
	v_mov_b32_e32 v116, v0
	v_mov_b32_e32 v117, v0
	v_mov_b32_e32 v118, v0
	v_mov_b32_e32 v119, v0
	v_mov_b32_e32 v72, v0
	v_mov_b32_e32 v73, v0
	v_mov_b32_e32 v74, v0
	v_mov_b32_e32 v75, v0
	v_mov_b32_e32 v76, v0
	v_mov_b32_e32 v77, v0
	v_mov_b32_e32 v78, v0
	v_mov_b32_e32 v79, v0
	v_mov_b32_e32 v88, v0
	v_mov_b32_e32 v89, v0
	v_mov_b32_e32 v90, v0
	v_mov_b32_e32 v91, v0
	v_mov_b32_e32 v92, v0
	v_mov_b32_e32 v93, v0
	v_mov_b32_e32 v94, v0
	v_mov_b32_e32 v95, v0
	v_mov_b32_e32 v104, v0
	v_mov_b32_e32 v105, v0
	v_mov_b32_e32 v106, v0
	v_mov_b32_e32 v107, v0
	v_mov_b32_e32 v108, v0
	v_mov_b32_e32 v109, v0
	v_mov_b32_e32 v110, v0
	v_mov_b32_e32 v111, v0
	v_mov_b32_e32 v120, v0
	v_mov_b32_e32 v121, v0
	v_mov_b32_e32 v122, v0
	v_mov_b32_e32 v123, v0
	v_mov_b32_e32 v124, v0
	v_mov_b32_e32 v125, v0
	v_mov_b32_e32 v126, v0
	v_mov_b32_e32 v127, v0

; template <class Epi, class Sched, bool ALIGN_EPI = false, bool SP2 = false, bool F8 = false, bool I8 = false, bool PF = false>
; __device__ __forceinline__ void gemm_phase(PG8_LAS unsigned char* lds, const Gemm g, const Sched& S, const Epi& E, const int wave_) {
;     ...
;         const char* nA = has_next ? (const char*)g.A + (size_t)nxt.pm * tstep : cA; const char* nB = has_next ? (const char*)g.Bt + (size_t)nxt.pb * tstep : cB;
;         for (int t = 0; t < nt; t += 2) {
;             const bool last = (t == nt - 2);
;             const char* a1 = cA + (size_t)(t + 1) * kstep;
;             const char* a2 = last ? nA : cA + (size_t)(t + 2) * kstep; const char* b2 = last ? nB : cB + (size_t)(t + 2) * kstep;
;     ...
; #pragma unroll
;         for (int a = 0; a < 2; ++a)
; #pragma unroll
;             for (int b = 0; b < 2; ++b)
; #pragma unroll
;                 for (int m = 0; m < 4; ++m)
; #pragma unroll
;                     for (int n = 0; n < 2; ++n) acc[a][b][m][n] = (f32x4){0.f, 0.f, 0.f, 0.f};
;         cur = nxt; cA = nA; cB = nB; ++ui;
.LBB0_670:
	s_add_u32 s63, s28, 0x100
	v_mov_b32_e32 v32, 0
	s_addc_u32 s64, s29, 0
	s_mov_b32 s65, -2
	v_mov_b32_e32 v33, v32
	v_mov_b32_e32 v34, v32
	v_mov_b32_e32 v35, v32
	v_mov_b32_e32 v36, v32
	v_mov_b32_e32 v37, v32
	v_mov_b32_e32 v38, v32
	v_mov_b32_e32 v39, v32
	v_mov_b32_e32 v48, v32
	v_mov_b32_e32 v49, v32
	v_mov_b32_e32 v50, v32
	v_mov_b32_e32 v51, v32
	v_mov_b32_e32 v52, v32
	v_mov_b32_e32 v53, v32
	v_mov_b32_e32 v54, v32
	v_mov_b32_e32 v55, v32
	v_mov_b32_e32 v64, v32
	v_mov_b32_e32 v65, v32
	v_mov_b32_e32 v66, v32
	v_mov_b32_e32 v67, v32
	v_mov_b32_e32 v68, v32
	v_mov_b32_e32 v69, v32
	v_mov_b32_e32 v70, v32
	v_mov_b32_e32 v71, v32
	v_mov_b32_e32 v80, v32
	v_mov_b32_e32 v81, v32
	v_mov_b32_e32 v82, v32
	v_mov_b32_e32 v83, v32
	v_mov_b32_e32 v84, v32
	v_mov_b32_e32 v85, v32
	v_mov_b32_e32 v86, v32
	v_mov_b32_e32 v87, v32
	v_mov_b32_e32 v40, v32
	v_mov_b32_e32 v41, v32
	v_mov_b32_e32 v42, v32
	v_mov_b32_e32 v43, v32
	v_mov_b32_e32 v44, v32
	v_mov_b32_e32 v45, v32
	v_mov_b32_e32 v46, v32
	v_mov_b32_e32 v47, v32
	v_mov_b32_e32 v56, v32
	v_mov_b32_e32 v57, v32
	v_mov_b32_e32 v58, v32
	v_mov_b32_e32 v59, v32
	v_mov_b32_e32 v60, v32
	v_mov_b32_e32 v61, v32
	v_mov_b32_e32 v62, v32
	v_mov_b32_e32 v63, v32
	v_mov_b32_e32 v72, v32
	v_mov_b32_e32 v73, v32
	v_mov_b32_e32 v74, v32
	v_mov_b32_e32 v75, v32
	v_mov_b32_e32 v76, v32
	v_mov_b32_e32 v77, v32
	v_mov_b32_e32 v78, v32
	v_mov_b32_e32 v79, v32
	v_mov_b32_e32 v88, v32
	v_mov_b32_e32 v89, v32
	v_mov_b32_e32 v90, v32
	v_mov_b32_e32 v91, v32
	v_mov_b32_e32 v92, v32
	v_mov_b32_e32 v93, v32
	v_mov_b32_e32 v94, v32
	v_mov_b32_e32 v95, v32
	v_mov_b32_e32 v96, v32
	v_mov_b32_e32 v97, v32
	v_mov_b32_e32 v98, v32
	v_mov_b32_e32 v99, v32
	v_mov_b32_e32 v100, v32
	v_mov_b32_e32 v101, v32
	v_mov_b32_e32 v102, v32
	v_mov_b32_e32 v103, v32
	v_mov_b32_e32 v112, v32
	v_mov_b32_e32 v113, v32
	v_mov_b32_e32 v114, v32
	v_mov_b32_e32 v115, v32
	v_mov_b32_e32 v116, v32
	v_mov_b32_e32 v117, v32
	v_mov_b32_e32 v118, v32
	v_mov_b32_e32 v119, v32
	v_mov_b32_e32 v128, v32
	v_mov_b32_e32 v129, v32
	v_mov_b32_e32 v130, v32
	v_mov_b32_e32 v131, v32
	v_mov_b32_e32 v132, v32
	v_mov_b32_e32 v133, v32
	v_mov_b32_e32 v134, v32
	v_mov_b32_e32 v135, v32
	v_mov_b32_e32 v144, v32
	v_mov_b32_e32 v145, v32
	v_mov_b32_e32 v146, v32
	v_mov_b32_e32 v147, v32
	v_mov_b32_e32 v148, v32
	v_mov_b32_e32 v149, v32
	v_mov_b32_e32 v150, v32
	v_mov_b32_e32 v151, v32
	v_mov_b32_e32 v104, v32
	v_mov_b32_e32 v105, v32
	v_mov_b32_e32 v106, v32
	v_mov_b32_e32 v107, v32
	v_mov_b32_e32 v108, v32
	v_mov_b32_e32 v109, v32
	v_mov_b32_e32 v110, v32
	v_mov_b32_e32 v111, v32
	v_mov_b32_e32 v120, v32
	v_mov_b32_e32 v121, v32
	v_mov_b32_e32 v122, v32
	v_mov_b32_e32 v123, v32
	v_mov_b32_e32 v124, v32
	v_mov_b32_e32 v125, v32
	v_mov_b32_e32 v126, v32
	v_mov_b32_e32 v127, v32
	v_mov_b32_e32 v136, v32
	v_mov_b32_e32 v137, v32
	v_mov_b32_e32 v138, v32
	v_mov_b32_e32 v139, v32
	v_mov_b32_e32 v140, v32
	v_mov_b32_e32 v141, v32
	v_mov_b32_e32 v142, v32
	v_mov_b32_e32 v143, v32
	v_mov_b32_e32 v152, v32
	v_mov_b32_e32 v153, v32
	v_mov_b32_e32 v154, v32
	v_mov_b32_e32 v155, v32
	v_mov_b32_e32 v156, v32
	v_mov_b32_e32 v157, v32
	v_mov_b32_e32 v158, v32
	v_mov_b32_e32 v159, v32

; template <class Epi, class Sched, bool ALIGN_EPI = false, bool SP2 = false, bool F8 = false, bool I8 = false, bool PF = false>
; __device__ __forceinline__ void gemm_phase(PG8_LAS unsigned char* lds, const Gemm g, const Sched& S, const Epi& E, const int wave_) {
;     ...
;         const bool has_next = S.next(ui + 1, nxt);
;         const char* nA = has_next ? (const char*)g.A + (size_t)nxt.pm * tstep : cA; const char* nB = has_next ? (const char*)g.Bt + (size_t)nxt.pb * tstep : cB;
;         for (int t = 0; t < nt; t += 2) {
;             const bool last = (t == nt - 2);
;             const char* a1 = cA + (size_t)(t + 1) * kstep;
;             const char* a2 = last ? nA : cA + (size_t)(t + 2) * kstep; const char* b2 = last ? nB : cB + (size_t)(t + 2) * kstep;
;     ...
; #pragma unroll
;         for (int a = 0; a < 2; ++a)
; #pragma unroll
;             for (int b = 0; b < 2; ++b)
; #pragma unroll
;                 for (int m = 0; m < 4; ++m)
; #pragma unroll
;                     for (int n = 0; n < 2; ++n) acc[a][b][m][n] = (f32x4){0.f, 0.f, 0.f, 0.f};
;         cur = nxt; cA = nA; cB = nB; ++ui;
.LBB0_808:
	s_ashr_i32 s19, s18, 31
	s_lshl_b64 s[22:23], s[18:19], 18
	s_add_u32 s22, s58, s22
	s_addc_u32 s23, s59, s23
	s_and_b64 s[26:27], s[20:21], exec
	s_cselect_b32 s19, s23, s31
	s_cselect_b32 s55, s22, s30
	s_ashr_i32 s17, s16, 31
	s_lshl_b64 s[26:27], s[16:17], 18
	s_add_u32 s26, s15, s26
	s_addc_u32 s27, s38, s27
	s_and_b64 s[36:37], s[20:21], exec
	s_cselect_b32 s17, s27, s35
	s_cselect_b32 s56, s26, s34
	s_add_u32 s30, s30, 0x20080
	s_addc_u32 s31, s31, 0
	s_add_u32 s57, s34, 0x100
	v_mov_b32_e32 v0, 0
	s_addc_u32 s62, s35, 0
	s_mov_b32 s63, -2
	v_mov_b32_e32 v1, v0
	v_mov_b32_e32 v2, v0
	v_mov_b32_e32 v3, v0
	v_mov_b32_e32 v4, v0
	v_mov_b32_e32 v5, v0
	v_mov_b32_e32 v6, v0
	v_mov_b32_e32 v7, v0
	v_mov_b32_e32 v16, v0
	v_mov_b32_e32 v17, v0
	v_mov_b32_e32 v18, v0
	v_mov_b32_e32 v19, v0
	v_mov_b32_e32 v20, v0
	v_mov_b32_e32 v21, v0
	v_mov_b32_e32 v22, v0
	v_mov_b32_e32 v23, v0
	v_mov_b32_e32 v32, v0
	v_mov_b32_e32 v33, v0
	v_mov_b32_e32 v34, v0
	v_mov_b32_e32 v35, v0
	v_mov_b32_e32 v36, v0
	v_mov_b32_e32 v37, v0
	v_mov_b32_e32 v38, v0
	v_mov_b32_e32 v39, v0
	v_mov_b32_e32 v48, v0
	v_mov_b32_e32 v49, v0
	v_mov_b32_e32 v50, v0
	v_mov_b32_e32 v51, v0
	v_mov_b32_e32 v52, v0
	v_mov_b32_e32 v53, v0
	v_mov_b32_e32 v54, v0
	v_mov_b32_e32 v55, v0
	v_mov_b32_e32 v8, v0
	v_mov_b32_e32 v9, v0
	v_mov_b32_e32 v10, v0
	v_mov_b32_e32 v11, v0
	v_mov_b32_e32 v12, v0
	v_mov_b32_e32 v13, v0
	v_mov_b32_e32 v14, v0
	v_mov_b32_e32 v15, v0
	v_mov_b32_e32 v24, v0
	v_mov_b32_e32 v25, v0
	v_mov_b32_e32 v26, v0
	v_mov_b32_e32 v27, v0
	v_mov_b32_e32 v28, v0
	v_mov_b32_e32 v29, v0
	v_mov_b32_e32 v30, v0
	v_mov_b32_e32 v31, v0
	v_mov_b32_e32 v40, v0
	v_mov_b32_e32 v41, v0
	v_mov_b32_e32 v42, v0
	v_mov_b32_e32 v43, v0
	v_mov_b32_e32 v44, v0
	v_mov_b32_e32 v45, v0
	v_mov_b32_e32 v46, v0
	v_mov_b32_e32 v47, v0
	v_mov_b32_e32 v56, v0
	v_mov_b32_e32 v57, v0
	v_mov_b32_e32 v58, v0
	v_mov_b32_e32 v59, v0
	v_mov_b32_e32 v60, v0
	v_mov_b32_e32 v61, v0
	v_mov_b32_e32 v62, v0
	v_mov_b32_e32 v63, v0
	v_mov_b32_e32 v64, v0
	v_mov_b32_e32 v65, v0
	v_mov_b32_e32 v66, v0
	v_mov_b32_e32 v67, v0
	v_mov_b32_e32 v68, v0
	v_mov_b32_e32 v69, v0
	v_mov_b32_e32 v70, v0
	v_mov_b32_e32 v71, v0
	v_mov_b32_e32 v80, v0
	v_mov_b32_e32 v81, v0
	v_mov_b32_e32 v82, v0
	v_mov_b32_e32 v83, v0
	v_mov_b32_e32 v84, v0
	v_mov_b32_e32 v85, v0
	v_mov_b32_e32 v86, v0
	v_mov_b32_e32 v87, v0
	v_mov_b32_e32 v96, v0
	v_mov_b32_e32 v97, v0
	v_mov_b32_e32 v98, v0
	v_mov_b32_e32 v99, v0
	v_mov_b32_e32 v100, v0
	v_mov_b32_e32 v101, v0
	v_mov_b32_e32 v102, v0
	v_mov_b32_e32 v103, v0
	v_mov_b32_e32 v112, v0
	v_mov_b32_e32 v113, v0
	v_mov_b32_e32 v114, v0
	v_mov_b32_e32 v115, v0
	v_mov_b32_e32 v116, v0
	v_mov_b32_e32 v117, v0
	v_mov_b32_e32 v118, v0
	v_mov_b32_e32 v119, v0
	v_mov_b32_e32 v72, v0
	v_mov_b32_e32 v73, v0
	v_mov_b32_e32 v74, v0
	v_mov_b32_e32 v75, v0
	v_mov_b32_e32 v76, v0
	v_mov_b32_e32 v77, v0
	v_mov_b32_e32 v78, v0
	v_mov_b32_e32 v79, v0
	v_mov_b32_e32 v88, v0
	v_mov_b32_e32 v89, v0
	v_mov_b32_e32 v90, v0
	v_mov_b32_e32 v91, v0
	v_mov_b32_e32 v92, v0
	v_mov_b32_e32 v93, v0
	v_mov_b32_e32 v94, v0
	v_mov_b32_e32 v95, v0
	v_mov_b32_e32 v104, v0
	v_mov_b32_e32 v105, v0
	v_mov_b32_e32 v106, v0
	v_mov_b32_e32 v107, v0
	v_mov_b32_e32 v108, v0
	v_mov_b32_e32 v109, v0
	v_mov_b32_e32 v110, v0
	v_mov_b32_e32 v111, v0
	v_mov_b32_e32 v120, v0
	v_mov_b32_e32 v121, v0
	v_mov_b32_e32 v122, v0
	v_mov_b32_e32 v123, v0
	v_mov_b32_e32 v124, v0
	v_mov_b32_e32 v125, v0
	v_mov_b32_e32 v126, v0
	v_mov_b32_e32 v127, v0

; template <class Epi, class Sched, bool ALIGN_EPI = false, bool SP2 = false, bool F8 = false, bool I8 = false, bool PF = false>
; __device__ __forceinline__ void gemm_phase(PG8_LAS unsigned char* lds, const Gemm g, const Sched& S, const Epi& E, const int wave_) {
;     ...
;         const bool has_next = S.next(ui + 1, nxt);
;         const char* nA = has_next ? (const char*)g.A + (size_t)nxt.pm * tstep : cA; const char* nB = has_next ? (const char*)g.Bt + (size_t)nxt.pb * tstep : cB;
;         for (int t = 0; t < nt; t += 2) {
;             const bool last = (t == nt - 2);
;             const char* a1 = cA + (size_t)(t + 1) * kstep;
;             const char* a2 = last ? nA : cA + (size_t)(t + 2) * kstep; const char* b2 = last ? nB : cB + (size_t)(t + 2) * kstep;
;     ...
; #pragma unroll
;         for (int a = 0; a < 2; ++a)
; #pragma unroll
;             for (int b = 0; b < 2; ++b)
; #pragma unroll
;                 for (int m = 0; m < 4; ++m)
; #pragma unroll
;                     for (int n = 0; n < 2; ++n) acc[a][b][m][n] = (f32x4){0.f, 0.f, 0.f, 0.f};
;         cur = nxt; cA = nA; cB = nB; ++ui;
.LBB0_966:
	s_ashr_i32 s27, s26, 31
	s_lshl_b64 s[30:31], s[26:27], 18
	s_add_u32 s30, s49, s30
	s_addc_u32 s31, s50, s31
	s_and_b64 s[34:35], s[28:29], exec
	s_cselect_b32 s5, s31, s39
	s_cselect_b32 s27, s30, s38
	s_ashr_i32 s23, s22, 31
	s_lshl_b64 s[34:35], s[22:23], 18
	s_add_u32 s34, s46, s34
	s_addc_u32 s35, s47, s35
	s_and_b64 s[42:43], s[28:29], exec
	s_cselect_b32 s23, s35, s41
	s_cselect_b32 s37, s34, s40
	s_add_u32 s38, s38, 0x20080
	s_addc_u32 s39, s39, 0
	s_add_u32 s70, s40, 0x100
	v_mov_b32_e32 v0, 0
	s_addc_u32 s71, s41, 0
	s_mov_b32 s72, -2
	v_mov_b32_e32 v1, v0
	v_mov_b32_e32 v2, v0
	v_mov_b32_e32 v3, v0
	v_mov_b32_e32 v4, v0
	v_mov_b32_e32 v5, v0
	v_mov_b32_e32 v6, v0
	v_mov_b32_e32 v7, v0
	v_mov_b32_e32 v16, v0
	v_mov_b32_e32 v17, v0
	v_mov_b32_e32 v18, v0
	v_mov_b32_e32 v19, v0
	v_mov_b32_e32 v20, v0
	v_mov_b32_e32 v21, v0
	v_mov_b32_e32 v22, v0
	v_mov_b32_e32 v23, v0
	v_mov_b32_e32 v32, v0
	v_mov_b32_e32 v33, v0
	v_mov_b32_e32 v34, v0
	v_mov_b32_e32 v35, v0
	v_mov_b32_e32 v36, v0
	v_mov_b32_e32 v37, v0
	v_mov_b32_e32 v38, v0
	v_mov_b32_e32 v39, v0
	v_mov_b32_e32 v48, v0
	v_mov_b32_e32 v49, v0
	v_mov_b32_e32 v50, v0
	v_mov_b32_e32 v51, v0
	v_mov_b32_e32 v52, v0
	v_mov_b32_e32 v53, v0
	v_mov_b32_e32 v54, v0
	v_mov_b32_e32 v55, v0
	v_mov_b32_e32 v8, v0
	v_mov_b32_e32 v9, v0
	v_mov_b32_e32 v10, v0
	v_mov_b32_e32 v11, v0
	v_mov_b32_e32 v12, v0
	v_mov_b32_e32 v13, v0
	v_mov_b32_e32 v14, v0
	v_mov_b32_e32 v15, v0
	v_mov_b32_e32 v24, v0
	v_mov_b32_e32 v25, v0
	v_mov_b32_e32 v26, v0
	v_mov_b32_e32 v27, v0
	v_mov_b32_e32 v28, v0
	v_mov_b32_e32 v29, v0
	v_mov_b32_e32 v30, v0
	v_mov_b32_e32 v31, v0
	v_mov_b32_e32 v40, v0
	v_mov_b32_e32 v41, v0
	v_mov_b32_e32 v42, v0
	v_mov_b32_e32 v43, v0
	v_mov_b32_e32 v44, v0
	v_mov_b32_e32 v45, v0
	v_mov_b32_e32 v46, v0
	v_mov_b32_e32 v47, v0
	v_mov_b32_e32 v56, v0
	v_mov_b32_e32 v57, v0
	v_mov_b32_e32 v58, v0
	v_mov_b32_e32 v59, v0
	v_mov_b32_e32 v60, v0
	v_mov_b32_e32 v61, v0
	v_mov_b32_e32 v62, v0
	v_mov_b32_e32 v63, v0
	v_mov_b32_e32 v64, v0
	v_mov_b32_e32 v65, v0
	v_mov_b32_e32 v66, v0
	v_mov_b32_e32 v67, v0
	v_mov_b32_e32 v68, v0
	v_mov_b32_e32 v69, v0
	v_mov_b32_e32 v70, v0
	v_mov_b32_e32 v71, v0
	v_mov_b32_e32 v80, v0
	v_mov_b32_e32 v81, v0
	v_mov_b32_e32 v82, v0
	v_mov_b32_e32 v83, v0
	v_mov_b32_e32 v84, v0
	v_mov_b32_e32 v85, v0
	v_mov_b32_e32 v86, v0
	v_mov_b32_e32 v87, v0
	v_mov_b32_e32 v96, v0
	v_mov_b32_e32 v97, v0
	v_mov_b32_e32 v98, v0
	v_mov_b32_e32 v99, v0
	v_mov_b32_e32 v100, v0
	v_mov_b32_e32 v101, v0
	v_mov_b32_e32 v102, v0
	v_mov_b32_e32 v103, v0
	v_mov_b32_e32 v112, v0
	v_mov_b32_e32 v113, v0
	v_mov_b32_e32 v114, v0
	v_mov_b32_e32 v115, v0
	v_mov_b32_e32 v116, v0
	v_mov_b32_e32 v117, v0
	v_mov_b32_e32 v118, v0
	v_mov_b32_e32 v119, v0
	v_mov_b32_e32 v72, v0
	v_mov_b32_e32 v73, v0
	v_mov_b32_e32 v74, v0
	v_mov_b32_e32 v75, v0
	v_mov_b32_e32 v76, v0
	v_mov_b32_e32 v77, v0
	v_mov_b32_e32 v78, v0
	v_mov_b32_e32 v79, v0
	v_mov_b32_e32 v88, v0
	v_mov_b32_e32 v89, v0
	v_mov_b32_e32 v90, v0
	v_mov_b32_e32 v91, v0
	v_mov_b32_e32 v92, v0
	v_mov_b32_e32 v93, v0
	v_mov_b32_e32 v94, v0
	v_mov_b32_e32 v95, v0
	v_mov_b32_e32 v104, v0
	v_mov_b32_e32 v105, v0
	v_mov_b32_e32 v106, v0
	v_mov_b32_e32 v107, v0
	v_mov_b32_e32 v108, v0
	v_mov_b32_e32 v109, v0
	v_mov_b32_e32 v110, v0
	v_mov_b32_e32 v111, v0
	v_mov_b32_e32 v120, v0
	v_mov_b32_e32 v121, v0
	v_mov_b32_e32 v122, v0
	v_mov_b32_e32 v123, v0
	v_mov_b32_e32 v124, v0
	v_mov_b32_e32 v125, v0
	v_mov_b32_e32 v126, v0
	v_mov_b32_e32 v127, v0

; __device__ __forceinline__ int crow(int r, int hi) { return (r & 3) + 8 * (r >> 2) + 4 * hi; }
; __device__ __forceinline__ unsigned cvtpk_s(float lo, float hi) { f32x2_t v = {lo, hi}; bf16x2_t b = __builtin_convertvector(v, bf16x2_t); return __builtin_bit_cast(unsigned, b); }
; __device__ __forceinline__ void unit(int b, int h, int qb, const unsigned short* Q, const unsigned short* KV, const unsigned short* KPE, unsigned short* O, char* shm, const int wave_) {
;     ...
;     { auto rr = __builtin_amdgcn_permlane32_swap(__float_as_uint(l), __float_as_uint(l), false, false); l = __uint_as_float(rr[0]) + __uint_as_float(rr[1]); }
;     if (hi == 0) wsf[32 + r32] = l; asm volatile("s_waitcnt lgkmcnt(0)" ::: "memory");
;     float rli[16];
; #pragma unroll
;     for (int r = 0; r < 16; ++r) rli[r] = __builtin_amdgcn_rcpf(wsf[32 + crow(r, hi)]);
;     unsigned short* Ow = O + (rowbase + q0 + wid * QBLK) * OP + 512 + h * 64;
;     { __attribute__((address_space(3))) unsigned short* stg = (__attribute__((address_space(3))) unsigned short*)((lds_cptr)shm + LDS_OST) + wid * 2048;
; #pragma unroll
;       for (int r = 0; r < 16; ++r) { const int orow = crow(r, hi);
; #pragma unroll
;           for (int d0 = 0; d0 < 2; ++d0) stg[orow * 64 + d0 * 32 + r32] = (unsigned short)(cvtpk_s(o[d0][r] * rli[r], 0.f) & 0xffffu); }
;       asm volatile("s_waitcnt lgkmcnt(0)" ::: "memory");
; #pragma unroll
;       for (int i = 0; i < 4; ++i) { const int row = i * 8 + (lane >> 3), ch = lane & 7; const u32x4 v = *(const __attribute__((address_space(3))) u32x4*)(stg + row * 64 + ch * 8); *(u32x4*)(Ow + (long)row * OP + ch * 8) = v; } }
;     asm volatile("s_waitcnt vmcnt(0) lgkmcnt(0)\n\ts_barrier" ::: "memory");
.LBB0_1086:
	s_or_b64 exec, exec, s[40:41]
	s_waitcnt lgkmcnt(0)
	ds_read_b128 v[34:37], v100 offset:61568
	ds_read_b128 v[38:41], v100 offset:61600
	s_lshl_b32 s2, s10, 12
	s_lshl_b64 s[0:1], s[0:1], 11
	s_add_i32 s2, s2, 0
	s_waitcnt lgkmcnt(1)
	v_rcp_f32_e32 v0, v34
	v_rcp_f32_e32 v42, v35
	v_lshlrev_b32_e32 v49, 9, v99
	v_lshlrev_b32_e32 v50, 1, v98
	v_mul_f32_e32 v18, v18, v0
	v_mul_f32_e32 v0, v2, v0
	v_add3_u32 v49, s2, v49, v50
	v_cvt_pk_bf16_f32 v0, v0, s0
	v_rcp_f32_e32 v43, v36
	ds_write_b16 v49, v0 offset:63552
	v_mul_f32_e32 v0, v19, v42
	v_cvt_pk_bf16_f32 v0, v0, s0
	ds_write_b16 v49, v0 offset:63616
	v_mul_f32_e32 v0, v3, v42
	v_cvt_pk_bf16_f32 v0, v0, s0
	v_rcp_f32_e32 v44, v37
	ds_write_b16 v49, v0 offset:63680
	v_mul_f32_e32 v0, v20, v43
	v_cvt_pk_bf16_f32 v0, v0, s0
	ds_write_b16 v49, v0 offset:63744
	v_mul_f32_e32 v0, v4, v43
	v_cvt_pk_bf16_f32 v0, v0, s0
	s_waitcnt lgkmcnt(4)
	v_rcp_f32_e32 v45, v38
	ds_write_b16 v49, v0 offset:63808
	v_mul_f32_e32 v0, v21, v44
	v_cvt_pk_bf16_f32 v0, v0, s0
	ds_write_b16 v49, v0 offset:63872
	v_mul_f32_e32 v0, v5, v44
	v_cvt_pk_bf16_f32 v0, v0, s0
	v_rcp_f32_e32 v46, v39
	ds_write_b16 v49, v0 offset:63936
	v_mul_f32_e32 v0, v22, v45
	v_cvt_pk_bf16_f32 v0, v0, s0
	ds_write_b16 v49, v0 offset:64512
	v_mul_f32_e32 v0, v6, v45
	v_cvt_pk_bf16_f32 v0, v0, s0
	v_rcp_f32_e32 v47, v40
	ds_write_b16 v49, v0 offset:64576
	v_mul_f32_e32 v0, v23, v46
	v_cvt_pk_bf16_f32 v0, v0, s0
	ds_write_b16 v49, v0 offset:64640
	v_mul_f32_e32 v0, v7, v46
	ds_read_b128 v[34:37], v100 offset:61632
	v_cvt_pk_bf16_f32 v0, v0, s0
	v_rcp_f32_e32 v48, v41
	ds_write_b16 v49, v0 offset:64704
	v_mul_f32_e32 v0, v24, v47
	v_cvt_pk_bf16_f32 v0, v0, s0
	ds_write_b16 v49, v0 offset:64768
	v_mul_f32_e32 v0, v8, v47
	v_cvt_pk_bf16_f32 v0, v0, s0
	ds_read_b128 v[38:41], v100 offset:61664
	s_waitcnt lgkmcnt(3)
	v_rcp_f32_e32 v34, v34
	ds_write_b16 v49, v0 offset:64832
	v_mul_f32_e32 v0, v25, v48
	v_cvt_pk_bf16_f32 v0, v0, s0
	ds_write_b16 v49, v0 offset:64896
	v_mul_f32_e32 v0, v9, v48
	v_cvt_pk_bf16_f32 v0, v0, s0
	v_rcp_f32_e32 v35, v35
	ds_write_b16 v49, v0 offset:64960
	v_mul_f32_e32 v0, v26, v34
	v_add_u32_e32 v50, 0xf800, v49
	v_cvt_pk_bf16_f32 v0, v0, s0
	ds_write_b16 v50, v0 offset:2048
	v_mul_f32_e32 v0, v10, v34
	v_cvt_pk_bf16_f32 v0, v0, s0
	v_rcp_f32_e32 v36, v36
	ds_write_b16 v50, v0 offset:2112
	v_mul_f32_e32 v0, v27, v35
	v_cvt_pk_bf16_f32 v0, v0, s0
	ds_write_b16 v50, v0 offset:2176
	v_mul_f32_e32 v0, v11, v35
	v_cvt_pk_bf16_f32 v0, v0, s0
	v_rcp_f32_e32 v37, v37
	ds_write_b16 v50, v0 offset:2240
	v_mul_f32_e32 v0, v28, v36
	v_cvt_pk_bf16_f32 v0, v0, s0
	ds_write_b16 v50, v0 offset:2304
	v_mul_f32_e32 v0, v12, v36
	v_cvt_pk_bf16_f32 v0, v0, s0
	s_waitcnt lgkmcnt(8)
	v_rcp_f32_e32 v38, v38
	ds_write_b16 v50, v0 offset:2368
	v_mul_f32_e32 v0, v29, v37
	v_cvt_pk_bf16_f32 v0, v0, s0
	ds_write_b16 v50, v0 offset:2432
	v_mul_f32_e32 v0, v13, v37
	v_cvt_pk_bf16_f32 v0, v0, s0
	v_rcp_f32_e32 v39, v39
	ds_write_b16 v50, v0 offset:2496
	v_mul_f32_e32 v0, v30, v38
	v_cvt_pk_bf16_f32 v0, v0, s0
	ds_write_b16 v50, v0 offset:3072
	v_mul_f32_e32 v0, v14, v38
	v_cvt_pk_bf16_f32 v0, v0, s0
	v_rcp_f32_e32 v40, v40
	ds_write_b16 v50, v0 offset:3136
	v_mul_f32_e32 v0, v31, v39
	v_cvt_pk_bf16_f32 v0, v0, s0
	ds_write_b16 v50, v0 offset:3200
	v_mul_f32_e32 v0, v15, v39
	v_cvt_pk_bf16_f32 v0, v0, s0
	v_rcp_f32_e32 v41, v41
	ds_write_b16 v50, v0 offset:3264
	v_mul_f32_e32 v0, v32, v40
	v_cvt_pk_bf16_f32 v0, v0, s0
	ds_write_b16 v50, v0 offset:3328
	v_mul_f32_e32 v0, v16, v40
	v_cvt_pk_bf16_f32 v0, v0, s0
	ds_write_b16 v50, v0 offset:3392
	v_mul_f32_e32 v0, v33, v41
	v_cvt_pk_bf16_f32 v0, v0, s0
	ds_write_b16 v50, v0 offset:3456
	v_mul_f32_e32 v0, v17, v41
	v_cvt_pk_bf16_f32 v0, v0, s0
	ds_write_b16 v50, v0 offset:3520
	v_lshlrev_b32_e32 v0, 1, v97
	v_cvt_pk_bf16_f32 v18, v18, s0
	s_add_u32 s0, s65, s0
	v_and_b32_e32 v0, 0x70, v0
	ds_write_b16 v49, v18 offset:63488
	s_addc_u32 s1, s66, s1
	v_lshrrev_b32_e32 v14, 3, v96
	v_add_u32_e32 v15, s2, v0
	s_waitcnt lgkmcnt(0)
	v_lshl_add_u64 v[10:11], s[0:1], 0, v[0:1]
	v_lshl_add_u32 v0, v14, 7, v15
	v_or_b32_e32 v16, 8, v14
	ds_read_b128 v[2:5], v0 offset:63488
	v_lshl_add_u32 v6, v16, 7, v15
	ds_read_b128 v[6:9], v6 offset:63488
	v_lshlrev_b32_e32 v0, 11, v14
	v_lshl_add_u64 v[12:13], v[10:11], 0, v[0:1]
	v_lshlrev_b32_e32 v0, 11, v16
	s_waitcnt lgkmcnt(1)
	global_store_dwordx4 v[12:13], v[2:5], off offset:1024
	s_nop 1
	v_lshl_add_u64 v[2:3], v[10:11], 0, v[0:1]
	v_or_b32_e32 v0, 16, v14
	s_waitcnt lgkmcnt(0)
	global_store_dwordx4 v[2:3], v[6:9], off offset:1024
	v_lshl_add_u32 v2, v0, 7, v15
	v_or_b32_e32 v14, 24, v14
	ds_read_b128 v[2:5], v2 offset:63488
	v_lshl_add_u32 v6, v14, 7, v15
	ds_read_b128 v[6:9], v6 offset:63488
	v_lshlrev_b32_e32 v0, 11, v0
	v_lshl_add_u64 v[12:13], v[10:11], 0, v[0:1]
	v_lshlrev_b32_e32 v0, 11, v14
	s_waitcnt lgkmcnt(1)
	global_store_dwordx4 v[12:13], v[2:5], off offset:1024
	s_nop 1
	v_lshl_add_u64 v[2:3], v[10:11], 0, v[0:1]
	s_waitcnt lgkmcnt(0)
	global_store_dwordx4 v[2:3], v[6:9], off offset:1024
	s_waitcnt lgkmcnt(0)
	s_barrier

; __device__ __forceinline__ int tid_from_wave(int wave) { unsigned l_; asm volatile("v_mbcnt_lo_u32_b32 %0, -1, 0\n\tv_mbcnt_hi_u32_b32 %0, -1, %0" : "=v"(l_)); return wave * 64 + (int)l_; }
; template <int THRL, bool LATE> __device__ __forceinline__ void unit_stag(int b, int h, int qb, const unsigned short* Q, const unsigned short* KV, const unsigned short* KPE, unsigned short* O, char* shm, const int wave_) {
;     int tid_ = tid_from_wave(wave_); asm volatile("" : "+v"(tid_));
;     const int tid = tid_, lane = tid & 63, r32 = lane & 31, hi = lane >> 5; const int wid = __builtin_amdgcn_readfirstlane(tid >> 6);
;     const long rowbase = (long)b * SEQ; const int q0 = qb * QB;
;     const unsigned short* Qw = Q + (rowbase + q0 + wid * QBLK) * QP + h * 96;
;     const unsigned short* Kh = KV + rowbase * KVP + h * 128; const unsigned short* Vh = Kh + 64; const unsigned short* Ph = KPE + rowbase * PEP;
;     const unsigned lds0 = (unsigned)(uintptr_t)shm;
;     __attribute__((address_space(3))) float* wsf = (__attribute__((address_space(3))) float*)((lds_cptr)shm + S4_WS) + wid * 64;
;     const unsigned short* ksrc = Kh + (long)lane * KVP + wid * 8;
;     const unsigned short* psrc = Ph + (long)(32 * (wid & 1) + r32) * PEP + (wid >> 1) * 8;
;     const unsigned short* vsrc = Vh + (long)(16 * (wid & 3) + (lane >> 2)) * KVP + (wid >> 2) * 32 + (lane & 3) * 8;
;     const unsigned kdst = lds0 + LDS_K + wid * 1024, pdst = lds0 + LDS_K + (8 + (wid >> 1)) * 1024 + (wid & 1) * 512, vdst = lds0 + S4_V + wid * 1024;
;     const int vb0 = (int)(lds0 + S4_V) + ((lane >> 4) & 1) * 32 + (lane & 3) * 8 + (4 * hi + ((lane & 15) >> 2)) * 64;
;     const lds_cptr kp0 = (lds_cptr)shm + LDS_K + hi * 1024 + r32 * 16;
;     const int NT = (q0 + QB) / KVBLK;
;     bf16x8 qr[6];
; #pragma unroll
;     for (int d0 = 0; d0 < 6; ++d0) qr[d0] = *reinterpret_cast<const bf16x8*>(&Qw[(long)r32 * QP + d0 * 16 + hi * 8]);
;     asm volatile("s_waitcnt vmcnt(0)" ::: "memory");
;     glds16(ksrc, (unsigned)__builtin_amdgcn_readfirstlane(kdst)); if (lane < 32) glds16(psrc, (unsigned)__builtin_amdgcn_readfirstlane(pdst));
.LBB0_1093:
	s_cmp_lg_u32 s2, 0
	s_cbranch_scc0 .LBB0_1123
	s_lshl_b32 s46, s2, 8
	s_add_u32 s47, s34, s46
	s_addc_u32 s69, s35, 0
	s_mov_b64 s[0:1], -1
	s_and_b64 vcc, exec, s[8:9]
	s_cbranch_vccz .LBB0_1145
	v_mbcnt_lo_u32_b32 v0, -1, 0
	v_mbcnt_hi_u32_b32 v0, -1, v0
	s_nop 0
	v_add_u32_e32 v82, s96, v0
	s_nop 0
	v_readfirstlane_b32 s10, v82
	s_ashr_i32 s68, s10, 6
	s_lshl_b32 s75, s68, 5
	s_ashr_i32 s0, s75, 31
	s_add_u32 s40, s47, s75
	s_addc_u32 s41, s69, s0
	v_and_b32_e32 v169, 31, v82
	s_mul_i32 s0, s41, 0x600
	s_mul_hi_u32 s1, s40, 0x600
	s_add_i32 s1, s1, s0
	s_mul_i32 s0, s40, 0x600
	v_mul_u32_u24_e32 v0, 0x300, v169
	v_bfe_u32 v170, v82, 5, 1
	s_add_u32 s0, s63, s0
	v_lshlrev_b32_e32 v0, 1, v0
	s_addc_u32 s1, s64, s1
	v_lshl_or_b32 v0, v170, 4, v0
	global_load_dwordx4 v[150:153], v0, s[0:1]
	global_load_dwordx4 v[146:149], v0, s[0:1] offset:32
	global_load_dwordx4 v[142:145], v0, s[0:1] offset:64
	global_load_dwordx4 v[138:141], v0, s[0:1] offset:96
	global_load_dwordx4 v[134:137], v0, s[0:1] offset:128
	global_load_dwordx4 v[130:133], v0, s[0:1] offset:160
	s_ashr_i32 s44, s10, 7
	s_lshl_b32 s0, s68, 3
	s_lshl_b32 s2, s44, 3
	v_and_b32_e32 v155, 63, v82
	s_ashr_i32 s1, s0, 31
	s_and_b32 s43, s68, 1
	s_ashr_i32 s3, s2, 31
	s_lshl_b32 s42, s68, 10
	s_lshl_b32 s44, s44, 10
	s_cmp_lg_u32 0, -1
	v_lshlrev_b32_e32 v0, 11, v155
	s_cselect_b32 s45, 0, 0
	v_lshl_add_u64 v[2:3], s[36:37], 0, v[0:1]
	v_lshlrev_b32_e32 v0, 6, v169
	s_add_i32 s44, s45, s44
	s_lshl_b32 s70, s43, 9
	v_lshl_add_u64 v[160:161], s[0:1], 1, v[2:3]
	v_lshl_or_b32 v0, s43, 11, v0
	s_add_i32 s76, s42, s45
	s_mov_b32 s0, m0
	s_mov_b32 m0, s76
	s_nop 0
	global_load_lds_dwordx4 v[160:161], off
	s_mov_b32 m0, s0
	s_add_i32 s71, s44, s70
	v_lshl_add_u64 v[2:3], s[38:39], 0, v[0:1]
	s_addk_i32 s71, 0x2000
	v_lshl_add_u64 v[158:159], s[2:3], 1, v[2:3]
	v_cmp_gt_u32_e64 s[2:3], 32, v155
	s_and_saveexec_b64 s[0:1], s[2:3]
	s_cbranch_execz .LBB0_1097
	s_mov_b32 s43, m0
	s_mov_b32 m0, s71
	s_nop 0
	global_load_lds_dwordx4 v[158:159], off
	s_mov_b32 m0, s43

; #define MLA_WAIT_BAR(N) asm volatile("s_waitcnt vmcnt(" #N ") lgkmcnt(0)\n\ts_barrier" ::: "memory")
; #define MLA_PIN(x) asm volatile("" : "+v"(x))
; #define MLA_LDK(kp, d0, h) (*(const __attribute__((address_space(3))) bf16x8*)((kp) + (d0) * 2048 + (h) * 512))
; #define MLA_MF(C, K, Q) C = __builtin_amdgcn_mfma_f32_32x32x16_bf16(K, Q, C, 0, 0, 0)
; template <int THRL, bool LATE> __device__ __forceinline__ void unit_stag(int b, int h, int qb, const unsigned short* Q, const unsigned short* KV, const unsigned short* KPE, unsigned short* O, char* shm, const int wave_) {
;     ...
;     glds16(ksrc, (unsigned)__builtin_amdgcn_readfirstlane(kdst)); if (lane < 32) glds16(psrc, (unsigned)__builtin_amdgcn_readfirstlane(pdst));
;     glds16(ksrc + (long)KVBLK * KVP, (unsigned)__builtin_amdgcn_readfirstlane(kdst + KSLOT)); if (lane < 32) glds16(psrc + (long)KVBLK * PEP, (unsigned)__builtin_amdgcn_readfirstlane(pdst + KSLOT)); glds16(vsrc, (unsigned)__builtin_amdgcn_readfirstlane(vdst));
;     glds16(ksrc + (long)2 * KVBLK * KVP, (unsigned)__builtin_amdgcn_readfirstlane(kdst + 2 * KSLOT)); if (lane < 32) glds16(psrc + (long)2 * KVBLK * PEP, (unsigned)__builtin_amdgcn_readfirstlane(pdst + 2 * KSLOT)); glds16(vsrc + (long)KVBLK * KVP, (unsigned)__builtin_amdgcn_readfirstlane(vdst + VSLOT));
;     float mhat = 0.f, l_reg = 0.f; f32x16 o[2]; o[0] = f32x16{}; o[1] = f32x16{}; f32x16 negm = f32x16{}; MLA_PIN(negm);
;     const int qrel = wid * QBLK + r32; bool resc = false;
;     f32x16 pA0, pA1, pB0, pB1; u32x4 pw0, pw1, pw2, pw3;
;     int s0 = 0, s1 = 1, s2 = 2;
;     MLA_WAIT_BAR(6);
;     { const lds_cptr kp = kp0;
;       pA0 = f32x16{}; pA1 = f32x16{};
; #pragma unroll
;       for (int d0 = 0; d0 < 6; ++d0) { const bf16x8 k0 = MLA_LDK(kp, d0, 0), k1 = MLA_LDK(kp, d0, 1); MLA_MF(pA0, k0, qr[d0]); MLA_MF(pA1, k1, qr[d0]); } }
;     { const float rm_ = rowmax(pA0, pA1); mhat = rm_;
; #pragma unroll
;       for (int r = 0; r < 16; ++r) { pA0[r] -= rm_; pA1[r] -= rm_; negm[r] = -mhat; }
;       MLA_PIN(negm); }
.LBB0_1101:
	s_or_b64 exec, exec, s[0:1]
	s_cmp_lg_u32 0, -1
	v_lshlrev_b32_e32 v0, 10, v170
	v_lshlrev_b32_e32 v2, 4, v169
	s_cselect_b32 s0, 0, 0
	v_add3_u32 v173, 0, v0, v2
	v_lshl_add_u64 v[2:3], v[156:157], 0, s[12:13]
	s_add_i32 s0, s0, s42
	s_add_i32 s0, s0, 0xb000
	s_mov_b32 s1, m0
	s_mov_b32 m0, s0
	s_nop 0
	global_load_lds_dwordx4 v[2:3], off
	s_mov_b32 m0, s1
	v_mov_b32_e32 v2, v1
	v_mov_b32_e32 v3, v1
	v_mov_b32_e32 v4, v1
	v_mov_b32_e32 v5, v1
	v_mov_b32_e32 v6, v1
	v_mov_b32_e32 v7, v1
	v_mov_b32_e32 v8, v1
	v_mov_b32_e32 v9, v1
	v_mov_b32_e32 v10, v1
	v_mov_b32_e32 v11, v1
	v_mov_b32_e32 v12, v1
	v_mov_b32_e32 v13, v1
	v_mov_b32_e32 v14, v1
	v_mov_b32_e32 v15, v1
	v_mov_b32_e32 v0, v1
	v_mov_b64_e32 v[16:17], v[14:15]
	v_mov_b64_e32 v[14:15], v[12:13]
	v_mov_b64_e32 v[12:13], v[10:11]
	v_mov_b64_e32 v[10:11], v[8:9]
	v_mov_b64_e32 v[8:9], v[6:7]
	v_mov_b64_e32 v[6:7], v[4:5]
	v_mov_b64_e32 v[4:5], v[2:3]
	v_mov_b64_e32 v[2:3], v[0:1]
	s_waitcnt vmcnt(6) lgkmcnt(0)
	s_barrier
	ds_read_b128 v[2:5], v173
	ds_read_b128 v[6:9], v173 offset:512
	s_waitcnt vmcnt(5) lgkmcnt(1)
	v_mfma_f32_32x32x16_bf16 v[18:33], v[2:5], v[150:153], 0
	ds_read_b128 v[34:37], v173 offset:2048
	ds_read_b128 v[38:41], v173 offset:2560
	v_lshl_add_u64 v[50:51], v[160:161], 0, s[22:23]
	s_waitcnt lgkmcnt(2)
	v_mfma_f32_32x32x16_bf16 v[2:17], v[6:9], v[150:153], 0
	s_waitcnt vmcnt(4) lgkmcnt(1)
	v_mfma_f32_32x32x16_bf16 v[18:33], v[34:37], v[146:149], v[18:33]
	s_waitcnt lgkmcnt(0)
	v_mfma_f32_32x32x16_bf16 v[2:17], v[38:41], v[146:149], v[2:17]
	ds_read_b128 v[34:37], v173 offset:4096
	ds_read_b128 v[38:41], v173 offset:4608
	s_waitcnt vmcnt(3) lgkmcnt(1)
	v_mfma_f32_32x32x16_bf16 v[18:33], v[34:37], v[142:145], v[18:33]
	s_waitcnt lgkmcnt(0)
	v_mfma_f32_32x32x16_bf16 v[2:17], v[38:41], v[142:145], v[2:17]
	ds_read_b128 v[34:37], v173 offset:6144
	ds_read_b128 v[38:41], v173 offset:6656
	s_waitcnt vmcnt(2) lgkmcnt(1)
	v_mfma_f32_32x32x16_bf16 v[18:33], v[34:37], v[138:141], v[18:33]
	s_waitcnt lgkmcnt(0)
	v_mfma_f32_32x32x16_bf16 v[2:17], v[38:41], v[138:141], v[2:17]
	ds_read_b128 v[34:37], v173 offset:8192
	ds_read_b128 v[38:41], v173 offset:8704
	s_waitcnt vmcnt(1) lgkmcnt(1)
	v_mfma_f32_32x32x16_bf16 v[18:33], v[34:37], v[134:137], v[18:33]
	s_waitcnt lgkmcnt(0)
	v_mfma_f32_32x32x16_bf16 v[2:17], v[38:41], v[134:137], v[2:17]
	ds_read_b128 v[34:37], v173 offset:10240
	ds_read_b128 v[38:41], v173 offset:10752
	s_waitcnt lgkmcnt(1)
	v_mfma_f32_32x32x16_bf16 v[18:33], v[34:37], v[130:133], v[18:33]
	s_waitcnt lgkmcnt(0)
	v_mfma_f32_32x32x16_bf16 v[2:17], v[38:41], v[130:133], v[2:17]
	v_max3_f32 v0, v18, v19, v2
	v_max3_f32 v34, v20, v21, v3
	s_nop 0
	v_max3_f32 v0, v0, v4, v5
	v_max3_f32 v34, v34, v24, v25
	s_nop 0
	v_max3_f32 v0, v0, v22, v23
	v_max3_f32 v34, v34, v8, v9
	s_nop 0
	v_max3_f32 v0, v0, v6, v7
	v_max3_f32 v34, v34, v28, v29
	s_nop 0
	v_max3_f32 v0, v0, v26, v27
	v_max3_f32 v34, v34, v12, v13
	s_nop 0
	v_max3_f32 v0, v0, v10, v11
	v_max3_f32 v34, v34, v32, v33
	s_nop 0
	v_max3_f32 v0, v0, v30, v31
	v_max3_f32 v34, v34, v16, v17
	s_nop 0
	v_max3_f32 v0, v0, v14, v15
	v_max_f32_e32 v34, v34, v34
	v_max_f32_e32 v0, v0, v0
	v_max_f32_e32 v0, v0, v34
	v_mov_b32_e32 v34, v0
	s_nop 1
	v_permlane32_swap_b32_e32 v0, v34
	v_max_f32_e32 v34, v34, v34
	v_max_f32_e32 v0, v0, v0
	v_max_f32_e32 v154, v0, v34
	v_xor_b32_e32 v34, 0x80000000, v154
	v_mov_b32_e32 v35, v34
	v_mov_b32_e32 v36, v34
	v_mov_b32_e32 v37, v34
	v_mov_b32_e32 v38, v34
	v_mov_b32_e32 v39, v34
	v_mov_b32_e32 v40, v34
	v_mov_b32_e32 v41, v34
	v_mov_b32_e32 v42, v34
	v_mov_b32_e32 v43, v34
	v_mov_b32_e32 v44, v34
	v_mov_b32_e32 v45, v34
	v_mov_b32_e32 v46, v34
	v_mov_b32_e32 v47, v34
	v_mov_b32_e32 v48, v34
	v_mov_b32_e32 v49, v34
	s_waitcnt vmcnt(3) lgkmcnt(0)
	s_barrier
	s_mov_b32 s0, m0
	s_mov_b32 m0, s76
	s_nop 0
	global_load_lds_dwordx4 v[50:51], off
	s_mov_b32 m0, s0
	s_and_saveexec_b64 s[0:1], s[2:3]
	s_cbranch_execz .LBB0_1103
	v_lshl_add_u64 v[50:51], v[158:159], 0, s[26:27]
	s_mov_b32 s43, m0
	s_mov_b32 m0, s71
	s_nop 0
	global_load_lds_dwordx4 v[50:51], off
	s_mov_b32 m0, s43

; __device__ __forceinline__ int crow(int r, int hi) { return (r & 3) + 8 * (r >> 2) + 4 * hi; }
; #define MLA_WAIT_BAR(N) asm volatile("s_waitcnt vmcnt(" #N ") lgkmcnt(0)\n\ts_barrier" ::: "memory")
; #define MLA_PVW(slot) pv(o, vb0 + (slot) * VSLOT, __builtin_bit_cast(bf16x8, pw0), __builtin_bit_cast(bf16x8, pw1), __builtin_bit_cast(bf16x8, pw2), __builtin_bit_cast(bf16x8, pw3))
; #define MLA_RESCB() do { if (resc) { asm volatile("s_waitcnt lgkmcnt(0)" ::: "memory"); _Pragma("unroll") for (int r = 0; r < 16; ++r) { const float g_ = wsf[crow(r, hi)]; o[0][r] *= g_; o[1][r] *= g_; } resc = false; } } while (0)
; template <int THRL, bool LATE> __device__ __forceinline__ void unit_stag(int b, int h, int qb, const unsigned short* Q, const unsigned short* KV, const unsigned short* KPE, unsigned short* O, char* shm, const int wave_) {
;     ...
;     MLA_WAIT_BAR(0);
;     if (LATE) { MLA_PVW((NT - 2) & 3); MLA_RESCB(); }
;     MLA_SOFT(pB0, pB1);
;     MLA_PVW((NT - 1) & 3);
;     { auto rr = __builtin_amdgcn_permlane32_swap(__float_as_uint(l_reg), __float_as_uint(l_reg), false, false); l_reg = __uint_as_float(rr[0]) + __uint_as_float(rr[1]); }
;     if (hi == 0) wsf[32 + r32] = l_reg; asm volatile("s_waitcnt lgkmcnt(0)" ::: "memory");
;     float rli[16];
; #pragma unroll
;     for (int r = 0; r < 16; ++r) rli[r] = __builtin_amdgcn_rcpf(wsf[32 + crow(r, hi)]);
.LBB0_1142:
	v_exp_f32_e32 v50, v50
	v_exp_f32_e32 v51, v51
	v_exp_f32_e32 v52, v52
	v_exp_f32_e32 v53, v53
	v_exp_f32_e32 v34, v34
	v_exp_f32_e32 v54, v54
	v_exp_f32_e32 v55, v55
	v_exp_f32_e32 v56, v56
	v_exp_f32_e32 v57, v57
	v_exp_f32_e32 v35, v35
	v_exp_f32_e32 v58, v58
	v_exp_f32_e32 v59, v59
	v_exp_f32_e32 v60, v60
	v_exp_f32_e32 v61, v61
	v_exp_f32_e32 v36, v36
	v_exp_f32_e32 v62, v62
	v_exp_f32_e32 v63, v63
	v_exp_f32_e32 v64, v64
	v_exp_f32_e32 v65, v65
	v_exp_f32_e32 v37, v37
	s_nop 0
	v_exp_f32_e32 v38, v38
	v_exp_f32_e32 v39, v39
	v_exp_f32_e32 v40, v40
	v_exp_f32_e32 v41, v41
	v_add_f32_e32 v66, 0, v50
	v_exp_f32_e32 v42, v42
	v_exp_f32_e32 v43, v43
	v_exp_f32_e32 v44, v44
	v_exp_f32_e32 v45, v45
	v_add_f32_e32 v66, v51, v66
	v_add_f32_e32 v66, v52, v66
	v_exp_f32_e32 v46, v46
	v_exp_f32_e32 v47, v47
	v_exp_f32_e32 v48, v48
	v_exp_f32_e32 v49, v49
	v_add_f32_e32 v66, v53, v66
	v_cvt_pk_bf16_f32 v114, v50, v51
	v_add_f32_e32 v66, v54, v66
	v_add_f32_e32 v66, v55, v66
	v_add_f32_e32 v66, v56, v66
	v_add_f32_e32 v66, v57, v66
	v_cvt_pk_bf16_f32 v115, v52, v53
	v_add_f32_e32 v66, v58, v66
	v_add_f32_e32 v66, v59, v66
	v_add_f32_e32 v66, v60, v66
	v_add_f32_e32 v66, v61, v66
	v_cvt_pk_bf16_f32 v118, v58, v59
	v_add_f32_e32 v66, v62, v66
	v_add_f32_e32 v66, v63, v66
	v_add_f32_e32 v66, v64, v66
	v_add_f32_e32 v66, v65, v66
	v_cvt_pk_bf16_f32 v119, v60, v61
	v_add_f32_e32 v66, v34, v66
	v_add_f32_e32 v66, v35, v66
	v_add_f32_e32 v66, v36, v66
	v_add_f32_e32 v66, v37, v66
	v_cvt_pk_bf16_f32 v122, v34, v35
	v_add_f32_e32 v66, v38, v66
	v_add_f32_e32 v66, v39, v66
	v_add_f32_e32 v66, v40, v66
	v_add_f32_e32 v66, v41, v66
	v_cvt_pk_bf16_f32 v123, v36, v37
	v_add_f32_e32 v66, v42, v66
	v_add_f32_e32 v66, v43, v66
	v_add_f32_e32 v66, v44, v66
	v_add_f32_e32 v66, v45, v66
	v_cvt_pk_bf16_f32 v126, v42, v43
	v_add_f32_e32 v66, v46, v66
	v_add_f32_e32 v66, v47, v66
	v_add_f32_e32 v66, v48, v66
	v_add_f32_e32 v66, v49, v66
	v_cvt_pk_bf16_f32 v127, v44, v45
	v_cvt_pk_bf16_f32 v116, v54, v55
	v_cvt_pk_bf16_f32 v117, v56, v57
	v_add_u32_e32 v35, 0x6000, v172
	v_cvt_pk_bf16_f32 v120, v62, v63
	v_cvt_pk_bf16_f32 v121, v64, v65
	v_add_f32_e32 v34, v98, v66
	v_cvt_pk_bf16_f32 v124, v38, v39
	v_cvt_pk_bf16_f32 v125, v40, v41
	s_nop 0
	v_cvt_pk_bf16_f32 v128, v46, v47
	v_cvt_pk_bf16_f32 v129, v48, v49
	ds_read_b64_tr_b16 v[36:37],v35 offset:0
	ds_read_b64_tr_b16 v[38:39],v35 offset:512
	ds_read_b64_tr_b16 v[40:41],v35 offset:1024
	ds_read_b64_tr_b16 v[42:43],v35 offset:1536
	ds_read_b64_tr_b16 v[44:45],v35 offset:2048
	ds_read_b64_tr_b16 v[46:47],v35 offset:2560
	ds_read_b64_tr_b16 v[48:49],v35 offset:3072
	ds_read_b64_tr_b16 v[50:51],v35 offset:3584
	s_waitcnt lgkmcnt(0)
	s_nop 0
	v_mfma_f32_32x32x16_bf16 v[18:33], v[114:117], v[36:39], v[18:33]
	ds_read_b64_tr_b16 v[36:37],v35 offset:4096
	ds_read_b64_tr_b16 v[38:39],v35 offset:4608
	v_mfma_f32_32x32x16_bf16 v[18:33], v[118:121], v[40:43], v[18:33]
	ds_read_b64_tr_b16 v[40:41],v35 offset:5120
	ds_read_b64_tr_b16 v[42:43],v35 offset:5632
	v_mfma_f32_32x32x16_bf16 v[18:33], v[122:125], v[44:47], v[18:33]
	ds_read_b64_tr_b16 v[44:45],v35 offset:6144
	ds_read_b64_tr_b16 v[46:47],v35 offset:6656
	ds_read_b64_tr_b16 v[52:53],v35 offset:7168
	ds_read_b64_tr_b16 v[54:55],v35 offset:7680
	s_waitcnt lgkmcnt(0)
	v_mfma_f32_32x32x16_bf16 v[18:33], v[126:129], v[48:51], v[18:33]
	v_mfma_f32_32x32x16_bf16 v[2:17], v[114:117], v[36:39], v[2:17]
	v_mov_b32_e32 v35, v34
	s_nop 1
	v_permlane32_swap_b32_e32 v34, v35
	v_mfma_f32_32x32x16_bf16 v[2:17], v[118:121], v[40:43], v[2:17]
	v_mfma_f32_32x32x16_bf16 v[2:17], v[122:125], v[44:47], v[2:17]
	v_mfma_f32_32x32x16_bf16 v[2:17], v[126:129], v[52:55], v[2:17]
	s_and_saveexec_b64 s[0:1], s[2:3]
	v_add_f32_e32 v34, v34, v35
	ds_write_b32 v171, v34 offset:128
	s_or_b64 exec, exec, s[0:1]
	s_waitcnt lgkmcnt(0)
	ds_read_b128 v[34:37], v181 offset:128
	ds_read_b128 v[38:41], v181 offset:160
	s_lshl_b32 s2, s68, 12
	s_add_i32 s2, s2, 0
	s_add_i32 s2, s2, 0x11800
	s_waitcnt lgkmcnt(1)
	v_rcp_f32_e32 v42, v34
	v_rcp_f32_e32 v43, v35
	s_lshl_b64 s[0:1], s[40:41], 11
	v_lshl_add_u32 v50, v169, 1, s2
	v_mul_f32_e32 v2, v2, v42
	v_rcp_f32_e32 v44, v36
	v_lshl_add_u32 v51, v170, 9, v50
	v_cvt_pk_bf16_f32 v2, v2, s0
	ds_write_b16 v51, v2 offset:64
	v_mul_f32_e32 v2, v19, v43
	v_cvt_pk_bf16_f32 v2, v2, s0
	ds_write_b16 v51, v2 offset:128
	v_mul_f32_e32 v2, v3, v43
	v_rcp_f32_e32 v45, v37
	v_cvt_pk_bf16_f32 v2, v2, s0
	v_mul_f32_e32 v3, v20, v44
	ds_write_b16 v51, v2 offset:192
	v_lshl_add_u32 v2, v179, 7, v50
	v_cvt_pk_bf16_f32 v3, v3, s0
	ds_write_b16 v2, v3
	v_mul_f32_e32 v3, v4, v44
	v_cvt_pk_bf16_f32 v3, v3, s0
	s_waitcnt lgkmcnt(4)
	v_rcp_f32_e32 v46, v38
	ds_write_b16 v2, v3 offset:64
	v_mul_f32_e32 v3, v21, v45
	v_lshl_add_u32 v2, v178, 7, v50
	v_cvt_pk_bf16_f32 v3, v3, s0
	ds_write_b16 v2, v3
	v_mul_f32_e32 v3, v5, v45
	v_cvt_pk_bf16_f32 v3, v3, s0
	v_rcp_f32_e32 v47, v39
	ds_write_b16 v2, v3 offset:64
	v_mul_f32_e32 v3, v22, v46
	v_lshl_add_u32 v2, v177, 7, v50
	v_cvt_pk_bf16_f32 v3, v3, s0
	ds_write_b16 v2, v3
	v_mul_f32_e32 v3, v6, v46
	v_cvt_pk_bf16_f32 v3, v3, s0
	v_rcp_f32_e32 v48, v40
	ds_write_b16 v2, v3 offset:64
	v_mul_f32_e32 v3, v23, v47
	v_lshl_add_u32 v2, v176, 7, v50
	v_cvt_pk_bf16_f32 v3, v3, s0
	ds_write_b16 v2, v3
	v_mul_f32_e32 v3, v7, v47
	ds_read_b128 v[34:37], v181 offset:192
	v_cvt_pk_bf16_f32 v3, v3, s0
	v_rcp_f32_e32 v49, v41
	ds_write_b16 v2, v3 offset:64
	v_mul_f32_e32 v3, v24, v48
	v_lshl_add_u32 v2, v175, 7, v50
	v_cvt_pk_bf16_f32 v3, v3, s0
	ds_write_b16 v2, v3
	v_mul_f32_e32 v3, v8, v48
	v_cvt_pk_bf16_f32 v3, v3, s0
	ds_read_b128 v[38:41], v181 offset:224
	s_waitcnt lgkmcnt(3)
; template <int THRL, bool LATE> __device__ __forceinline__ void unit_stag(int b, int h, int qb, const unsigned short* Q, const unsigned short* KV, const unsigned short* KPE, unsigned short* O, char* shm, const int wave_) {
;     int tid_ = tid_from_wave(wave_); asm volatile("" : "+v"(tid_));
;     const int tid = tid_, lane = tid & 63, r32 = lane & 31, hi = lane >> 5; const int wid = __builtin_amdgcn_readfirstlane(tid >> 6);
;     const long rowbase = (long)b * SEQ; const int q0 = qb * QB;
;     const unsigned short* Qw = Q + (rowbase + q0 + wid * QBLK) * QP + h * 96;
;     const unsigned short* Kh = KV + rowbase * KVP + h * 128; const unsigned short* Vh = Kh + 64; const unsigned short* Ph = KPE + rowbase * PEP;
;     const unsigned lds0 = (unsigned)(uintptr_t)shm;
;     __attribute__((address_space(3))) float* wsf = (__attribute__((address_space(3))) float*)((lds_cptr)shm + S4_WS) + wid * 64;
;     const unsigned short* ksrc = Kh + (long)lane * KVP + wid * 8;
;     const unsigned short* psrc = Ph + (long)(32 * (wid & 1) + r32) * PEP + (wid >> 1) * 8;
;     const unsigned short* vsrc = Vh + (long)(16 * (wid & 3) + (lane >> 2)) * KVP + (wid >> 2) * 32 + (lane & 3) * 8;
;     const unsigned kdst = lds0 + LDS_K + wid * 1024, pdst = lds0 + LDS_K + (8 + (wid >> 1)) * 1024 + (wid & 1) * 512, vdst = lds0 + S4_V + wid * 1024;
;     const int vb0 = (int)(lds0 + S4_V) + ((lane >> 4) & 1) * 32 + (lane & 3) * 8 + (4 * hi + ((lane & 15) >> 2)) * 64;
;     const lds_cptr kp0 = (lds_cptr)shm + LDS_K + hi * 1024 + r32 * 16;
;     ...
;     unsigned short* Ow = O + (rowbase + q0 + wid * QBLK) * OP + 512 + h * 64;
;     { __attribute__((address_space(3))) unsigned short* stg = (__attribute__((address_space(3))) unsigned short*)((lds_cptr)shm + S4_OST) + wid * 2048;
; #pragma unroll
;       for (int r = 0; r < 16; ++r) { const int orow = crow(r, hi);
; #pragma unroll
;           for (int d0 = 0; d0 < 2; ++d0) stg[orow * 64 + d0 * 32 + r32] = (unsigned short)(cvtpk_s(o[d0][r] * rli[r], 0.f) & 0xffffu); }
;       asm volatile("s_waitcnt lgkmcnt(0)" ::: "memory");
; #pragma unroll
;       for (int i = 0; i < 4; ++i) { const int row = i * 8 + (lane >> 3), ch = lane & 7; const u32x4 v = *(const __attribute__((address_space(3))) u32x4*)(stg + row * 64 + ch * 8); *(u32x4*)(Ow + (long)row * OP + ch * 8) = v; } }
;     asm volatile("s_waitcnt vmcnt(0) lgkmcnt(0)\n\ts_barrier" ::: "memory");
	v_rcp_f32_e32 v34, v34
	ds_write_b16 v2, v3 offset:64
	v_mul_f32_e32 v3, v25, v49
	v_lshl_add_u32 v2, v174, 7, v50
	v_cvt_pk_bf16_f32 v3, v3, s0
	ds_write_b16 v2, v3
	v_mul_f32_e32 v3, v9, v49
	v_cvt_pk_bf16_f32 v3, v3, s0
	v_rcp_f32_e32 v35, v35
	ds_write_b16 v2, v3 offset:64
	v_mul_f32_e32 v3, v26, v34
	v_lshl_add_u32 v2, v173, 7, v50
	v_cvt_pk_bf16_f32 v3, v3, s0
	ds_write_b16 v2, v3
	v_mul_f32_e32 v3, v10, v34
	v_cvt_pk_bf16_f32 v3, v3, s0
	v_rcp_f32_e32 v36, v36
	ds_write_b16 v2, v3 offset:64
	v_mul_f32_e32 v3, v27, v35
	v_lshl_add_u32 v2, v167, 7, v50
	v_cvt_pk_bf16_f32 v3, v3, s0
	ds_write_b16 v2, v3
	v_mul_f32_e32 v3, v11, v35
	v_cvt_pk_bf16_f32 v3, v3, s0
	v_rcp_f32_e32 v37, v37
	ds_write_b16 v2, v3 offset:64
	v_mul_f32_e32 v3, v28, v36
	v_lshl_add_u32 v2, v166, 7, v50
	v_cvt_pk_bf16_f32 v3, v3, s0
	ds_write_b16 v2, v3
	v_mul_f32_e32 v3, v12, v36
	v_cvt_pk_bf16_f32 v3, v3, s0
	s_waitcnt lgkmcnt(8)
	v_rcp_f32_e32 v38, v38
	ds_write_b16 v2, v3 offset:64
	v_mul_f32_e32 v3, v29, v37
	v_lshl_add_u32 v2, v165, 7, v50
	v_cvt_pk_bf16_f32 v3, v3, s0
	ds_write_b16 v2, v3
	v_mul_f32_e32 v3, v13, v37
	v_cvt_pk_bf16_f32 v3, v3, s0
	v_rcp_f32_e32 v39, v39
	ds_write_b16 v2, v3 offset:64
	v_mul_f32_e32 v3, v30, v38
	v_lshl_add_u32 v2, v164, 7, v50
	v_cvt_pk_bf16_f32 v3, v3, s0
	ds_write_b16 v2, v3
	v_mul_f32_e32 v3, v14, v38
	v_cvt_pk_bf16_f32 v3, v3, s0
	v_rcp_f32_e32 v40, v40
	ds_write_b16 v2, v3 offset:64
	v_mul_f32_e32 v3, v31, v39
	v_lshl_add_u32 v2, v163, 7, v50
	v_cvt_pk_bf16_f32 v3, v3, s0
	ds_write_b16 v2, v3
	v_mul_f32_e32 v3, v15, v39
	v_cvt_pk_bf16_f32 v3, v3, s0
	v_rcp_f32_e32 v41, v41
	ds_write_b16 v2, v3 offset:64
	v_mul_f32_e32 v3, v32, v40
	v_lshl_add_u32 v2, v162, 7, v50
	v_cvt_pk_bf16_f32 v3, v3, s0
	ds_write_b16 v2, v3
	v_mul_f32_e32 v3, v16, v40
	v_cvt_pk_bf16_f32 v3, v3, s0
	ds_write_b16 v2, v3 offset:64
	v_mul_f32_e32 v2, v33, v41
	v_lshl_add_u32 v0, v0, 7, v50
	v_cvt_pk_bf16_f32 v2, v2, s0
	ds_write_b16 v0, v2
	v_mul_f32_e32 v2, v17, v41
	v_cvt_pk_bf16_f32 v2, v2, s0
	v_mul_f32_e32 v18, v18, v42
	ds_write_b16 v0, v2 offset:64
	v_lshlrev_b32_e32 v0, 1, v168
	v_cvt_pk_bf16_f32 v18, v18, s0
	s_add_u32 s0, s65, s0
	v_and_b32_e32 v0, 0x70, v0
	ds_write_b16 v51, v18
	s_addc_u32 s1, s66, s1
	v_lshrrev_b32_e32 v14, 3, v155
	v_add_u32_e32 v15, s2, v0
	s_waitcnt lgkmcnt(0)
	v_lshl_add_u64 v[10:11], s[0:1], 0, v[0:1]
	v_lshl_add_u32 v0, v14, 7, v15
	v_or_b32_e32 v16, 8, v14
	ds_read_b128 v[2:5], v0
	v_lshl_add_u32 v6, v16, 7, v15
	ds_read_b128 v[6:9], v6
	v_lshlrev_b32_e32 v0, 11, v14
	v_lshl_add_u64 v[12:13], v[10:11], 0, v[0:1]
	v_lshlrev_b32_e32 v0, 11, v16
	s_waitcnt lgkmcnt(1)
	global_store_dwordx4 v[12:13], v[2:5], off offset:1024
	s_mov_b64 s[0:1], 0
	s_nop 0
	v_lshl_add_u64 v[2:3], v[10:11], 0, v[0:1]
	v_or_b32_e32 v0, 16, v14
	s_waitcnt lgkmcnt(0)
	global_store_dwordx4 v[2:3], v[6:9], off offset:1024
	v_lshl_add_u32 v2, v0, 7, v15
	v_or_b32_e32 v14, 24, v14
	ds_read_b128 v[2:5], v2
	v_lshl_add_u32 v6, v14, 7, v15
	ds_read_b128 v[6:9], v6
	v_lshlrev_b32_e32 v0, 11, v0
	v_lshl_add_u64 v[12:13], v[10:11], 0, v[0:1]
	v_lshlrev_b32_e32 v0, 11, v14
	s_waitcnt lgkmcnt(1)
	global_store_dwordx4 v[12:13], v[2:5], off offset:1024
	s_nop 1
	v_lshl_add_u64 v[2:3], v[10:11], 0, v[0:1]
	s_waitcnt lgkmcnt(0)
	global_store_dwordx4 v[2:3], v[6:9], off offset:1024
	s_waitcnt lgkmcnt(0)
	s_barrier
.LBB0_1145:
	s_and_b64 vcc, exec, s[0:1]
	s_cbranch_vccz .LBB0_1172
	v_mbcnt_lo_u32_b32 v0, -1, 0
	v_mbcnt_hi_u32_b32 v0, -1, v0
	s_nop 0
	v_add_u32_e32 v34, s96, v0
	s_nop 0
	v_readfirstlane_b32 s10, v34
	s_ashr_i32 s68, s10, 6
	s_lshl_b32 s75, s68, 5
	s_ashr_i32 s0, s75, 31
	s_add_u32 s40, s47, s75
	s_addc_u32 s41, s69, s0
	v_and_b32_e32 v209, 31, v34
	s_mul_i32 s0, s41, 0x600
	s_mul_hi_u32 s1, s40, 0x600
	s_add_i32 s1, s1, s0
	s_mul_i32 s0, s40, 0x600
	v_mul_u32_u24_e32 v0, 0x300, v209
	v_bfe_u32 v210, v34, 5, 1
	s_add_u32 s0, s63, s0
	v_lshlrev_b32_e32 v0, 1, v0
	s_addc_u32 s1, s64, s1
	v_lshl_or_b32 v0, v210, 4, v0
	global_load_dwordx4 v[196:199], v0, s[0:1]
	global_load_dwordx4 v[192:195], v0, s[0:1] offset:32
	global_load_dwordx4 v[188:191], v0, s[0:1] offset:64
	global_load_dwordx4 v[184:187], v0, s[0:1] offset:96
	global_load_dwordx4 v[180:183], v0, s[0:1] offset:128
	global_load_dwordx4 v[176:179], v0, s[0:1] offset:160
	s_ashr_i32 s44, s10, 7
	s_lshl_b32 s0, s68, 3
	s_lshl_b32 s2, s44, 3
	s_ashr_i32 s1, s0, 31
	s_and_b32 s43, s68, 1
	s_ashr_i32 s3, s2, 31
	s_lshl_b32 s42, s68, 10
	s_lshl_b32 s44, s44, 10
	v_and_b32_e32 v207, 63, v34
	s_cmp_lg_u32 0, -1
	s_cselect_b32 s45, 0, 0
	v_lshlrev_b32_e32 v0, 11, v207
	s_add_i32 s44, s45, s44
	s_lshl_b32 s47, s43, 9
	v_lshl_add_u64 v[2:3], s[36:37], 0, v[0:1]
	v_lshlrev_b32_e32 v0, 6, v209
	s_add_i32 s70, s44, s47
	v_lshl_add_u64 v[204:205], s[0:1], 1, v[2:3]
	v_lshl_or_b32 v0, s43, 11, v0
	s_add_i32 s44, s42, s45
	s_mov_b32 s0, m0
	s_mov_b32 m0, s44
	s_nop 0
	global_load_lds_dwordx4 v[204:205], off
	s_mov_b32 m0, s0
	v_lshl_add_u64 v[2:3], s[38:39], 0, v[0:1]
	s_addk_i32 s70, 0x2000
	v_lshl_add_u64 v[202:203], s[2:3], 1, v[2:3]
	v_cmp_gt_u32_e64 s[2:3], 32, v207
	s_and_saveexec_b64 s[0:1], s[2:3]
	s_cbranch_execz .LBB0_1148
	s_mov_b32 s43, m0
	s_mov_b32 m0, s70
	s_nop 0
	global_load_lds_dwordx4 v[202:203], off
	s_mov_b32 m0, s43

; #define MLA_WAIT_BAR(N) asm volatile("s_waitcnt vmcnt(" #N ") lgkmcnt(0)\n\ts_barrier" ::: "memory")
; #define MLA_PIN(x) asm volatile("" : "+v"(x))
; #define MLA_LDK(kp, d0, h) (*(const __attribute__((address_space(3))) bf16x8*)((kp) + (d0) * 2048 + (h) * 512))
; #define MLA_MF(C, K, Q) C = __builtin_amdgcn_mfma_f32_32x32x16_bf16(K, Q, C, 0, 0, 0)
; template <int THRL, bool LATE> __device__ __forceinline__ void unit_stag(int b, int h, int qb, const unsigned short* Q, const unsigned short* KV, const unsigned short* KPE, unsigned short* O, char* shm, const int wave_) {
;     ...
;     glds16(ksrc, (unsigned)__builtin_amdgcn_readfirstlane(kdst)); if (lane < 32) glds16(psrc, (unsigned)__builtin_amdgcn_readfirstlane(pdst));
;     glds16(ksrc + (long)KVBLK * KVP, (unsigned)__builtin_amdgcn_readfirstlane(kdst + KSLOT)); if (lane < 32) glds16(psrc + (long)KVBLK * PEP, (unsigned)__builtin_amdgcn_readfirstlane(pdst + KSLOT)); glds16(vsrc, (unsigned)__builtin_amdgcn_readfirstlane(vdst));
;     glds16(ksrc + (long)2 * KVBLK * KVP, (unsigned)__builtin_amdgcn_readfirstlane(kdst + 2 * KSLOT)); if (lane < 32) glds16(psrc + (long)2 * KVBLK * PEP, (unsigned)__builtin_amdgcn_readfirstlane(pdst + 2 * KSLOT)); glds16(vsrc + (long)KVBLK * KVP, (unsigned)__builtin_amdgcn_readfirstlane(vdst + VSLOT));
;     float mhat = 0.f, l_reg = 0.f; f32x16 o[2]; o[0] = f32x16{}; o[1] = f32x16{}; f32x16 negm = f32x16{}; MLA_PIN(negm);
;     const int qrel = wid * QBLK + r32; bool resc = false;
;     f32x16 pA0, pA1, pB0, pB1; u32x4 pw0, pw1, pw2, pw3;
;     int s0 = 0, s1 = 1, s2 = 2;
;     MLA_WAIT_BAR(6);
;     { const lds_cptr kp = kp0;
;       pA0 = f32x16{}; pA1 = f32x16{};
; #pragma unroll
;       for (int d0 = 0; d0 < 6; ++d0) { const bf16x8 k0 = MLA_LDK(kp, d0, 0), k1 = MLA_LDK(kp, d0, 1); MLA_MF(pA0, k0, qr[d0]); MLA_MF(pA1, k1, qr[d0]); } }
;     { const float rm_ = rowmax(pA0, pA1); mhat = rm_;
; #pragma unroll
;       for (int r = 0; r < 16; ++r) { pA0[r] -= rm_; pA1[r] -= rm_; negm[r] = -mhat; }
;       MLA_PIN(negm); }
.LBB0_1152:
	s_or_b64 exec, exec, s[0:1]
	s_cmp_lg_u32 0, -1
	v_lshlrev_b32_e32 v0, 10, v210
	v_lshlrev_b32_e32 v2, 4, v209
	s_cselect_b32 s0, 0, 0
	v_add3_u32 v213, 0, v0, v2
	v_lshl_add_u64 v[2:3], v[200:201], 0, s[12:13]
	s_add_i32 s0, s0, s42
	s_add_i32 s0, s0, 0xb000
	s_mov_b32 s1, m0
	s_mov_b32 m0, s0
	s_nop 0
	global_load_lds_dwordx4 v[2:3], off
	s_mov_b32 m0, s1
	v_mov_b32_e32 v2, v1
	v_mov_b32_e32 v3, v1
	v_mov_b32_e32 v4, v1
	v_mov_b32_e32 v5, v1
	v_mov_b32_e32 v6, v1
	v_mov_b32_e32 v7, v1
	v_mov_b32_e32 v8, v1
	v_mov_b32_e32 v9, v1
	v_mov_b32_e32 v10, v1
	v_mov_b32_e32 v11, v1
	v_mov_b32_e32 v12, v1
	v_mov_b32_e32 v13, v1
	v_mov_b32_e32 v14, v1
	v_mov_b32_e32 v15, v1
	v_mov_b32_e32 v0, v1
	v_mov_b64_e32 v[16:17], v[14:15]
	v_mov_b64_e32 v[14:15], v[12:13]
	v_mov_b64_e32 v[12:13], v[10:11]
	v_mov_b64_e32 v[10:11], v[8:9]
	v_mov_b64_e32 v[8:9], v[6:7]
	v_mov_b64_e32 v[6:7], v[4:5]
	v_mov_b64_e32 v[4:5], v[2:3]
	v_mov_b64_e32 v[2:3], v[0:1]
	s_waitcnt vmcnt(6) lgkmcnt(0)
	s_barrier
	ds_read_b128 v[2:5], v213
	ds_read_b128 v[6:9], v213 offset:512
	s_waitcnt vmcnt(5) lgkmcnt(1)
	v_mfma_f32_32x32x16_bf16 v[18:33], v[2:5], v[196:199], 0
	ds_read_b128 v[36:39], v213 offset:2048
	ds_read_b128 v[40:43], v213 offset:2560
	s_waitcnt lgkmcnt(2)
	v_mfma_f32_32x32x16_bf16 v[2:17], v[6:9], v[196:199], 0
	s_waitcnt vmcnt(4) lgkmcnt(1)
	v_mfma_f32_32x32x16_bf16 v[18:33], v[36:39], v[192:195], v[18:33]
	s_waitcnt lgkmcnt(0)
	v_mfma_f32_32x32x16_bf16 v[2:17], v[40:43], v[192:195], v[2:17]
	ds_read_b128 v[36:39], v213 offset:4096
	ds_read_b128 v[40:43], v213 offset:4608
	s_waitcnt vmcnt(3) lgkmcnt(1)
	v_mfma_f32_32x32x16_bf16 v[18:33], v[36:39], v[188:191], v[18:33]
	s_waitcnt lgkmcnt(0)
	v_mfma_f32_32x32x16_bf16 v[2:17], v[40:43], v[188:191], v[2:17]
	ds_read_b128 v[36:39], v213 offset:6144
	ds_read_b128 v[40:43], v213 offset:6656
	s_waitcnt vmcnt(2) lgkmcnt(1)
	v_mfma_f32_32x32x16_bf16 v[18:33], v[36:39], v[184:187], v[18:33]
	s_waitcnt lgkmcnt(0)
	v_mfma_f32_32x32x16_bf16 v[2:17], v[40:43], v[184:187], v[2:17]
	ds_read_b128 v[36:39], v213 offset:8192
	ds_read_b128 v[40:43], v213 offset:8704
	s_waitcnt vmcnt(1) lgkmcnt(1)
	v_mfma_f32_32x32x16_bf16 v[18:33], v[36:39], v[180:183], v[18:33]
	s_waitcnt lgkmcnt(0)
	v_mfma_f32_32x32x16_bf16 v[2:17], v[40:43], v[180:183], v[2:17]
	ds_read_b128 v[36:39], v213 offset:10240
	ds_read_b128 v[40:43], v213 offset:10752
	s_waitcnt lgkmcnt(1)
	v_mfma_f32_32x32x16_bf16 v[18:33], v[36:39], v[176:179], v[18:33]
	s_waitcnt lgkmcnt(0)
	v_mfma_f32_32x32x16_bf16 v[2:17], v[40:43], v[176:179], v[2:17]
	v_max3_f32 v0, v18, v19, v2
	v_max3_f32 v36, v20, v21, v3
	s_nop 0
	v_max3_f32 v0, v0, v4, v5
	v_max3_f32 v36, v36, v24, v25
	s_nop 0
	v_max3_f32 v0, v0, v22, v23
	v_max3_f32 v36, v36, v8, v9
	s_nop 0
	v_max3_f32 v0, v0, v6, v7
	v_max3_f32 v36, v36, v28, v29
	s_nop 0
	v_max3_f32 v0, v0, v26, v27
	v_max3_f32 v36, v36, v12, v13
	s_nop 0
	v_max3_f32 v0, v0, v10, v11
	v_max3_f32 v36, v36, v32, v33
	s_nop 0
	v_max3_f32 v0, v0, v30, v31
	v_max3_f32 v36, v36, v16, v17
	s_nop 0
	v_max3_f32 v0, v0, v14, v15
	v_max_f32_e32 v36, v36, v36
	v_max_f32_e32 v0, v0, v0
	v_max_f32_e32 v0, v0, v36
	v_mov_b32_e32 v36, v0
	s_nop 1
	v_permlane32_swap_b32_e32 v0, v36
	v_max_f32_e32 v36, v36, v36
	v_max_f32_e32 v0, v0, v0
	v_max_f32_e32 v0, v0, v36
	v_xor_b32_e32 v82, 0x80000000, v0
	v_mov_b32_e32 v83, v82
	v_mov_b32_e32 v84, v82
	v_mov_b32_e32 v85, v82
	v_mov_b32_e32 v86, v82
	v_mov_b32_e32 v87, v82
	v_mov_b32_e32 v88, v82
	v_mov_b32_e32 v89, v82
	v_mov_b32_e32 v90, v82
	v_mov_b32_e32 v91, v82
	v_mov_b32_e32 v92, v82
	v_mov_b32_e32 v93, v82
	v_mov_b32_e32 v94, v82
	v_mov_b32_e32 v95, v82
	v_mov_b32_e32 v96, v82
	v_mov_b32_e32 v97, v82
	s_waitcnt vmcnt(3) lgkmcnt(0)
	s_barrier
	v_sub_f32_e32 v48, v2, v0
	v_sub_f32_e32 v2, v19, v0
	v_sub_f32_e32 v18, v18, v0
	v_sub_f32_e32 v49, v3, v0
	v_sub_f32_e32 v3, v20, v0
	v_sub_f32_e32 v50, v4, v0
	v_sub_f32_e32 v4, v21, v0
	v_sub_f32_e32 v51, v5, v0
	v_pk_add_f32 v[22:23], v[22:23], v[0:1] op_sel_hi:[1,0] neg_lo:[0,1] neg_hi:[0,1]
	v_pk_add_f32 v[6:7], v[6:7], v[0:1] op_sel_hi:[1,0] neg_lo:[0,1] neg_hi:[0,1]
	v_pk_add_f32 v[24:25], v[24:25], v[0:1] op_sel_hi:[1,0] neg_lo:[0,1] neg_hi:[0,1]
	v_pk_add_f32 v[8:9], v[8:9], v[0:1] op_sel_hi:[1,0] neg_lo:[0,1] neg_hi:[0,1]
	v_pk_add_f32 v[26:27], v[26:27], v[0:1] op_sel_hi:[1,0] neg_lo:[0,1] neg_hi:[0,1]
	v_pk_add_f32 v[10:11], v[10:11], v[0:1] op_sel_hi:[1,0] neg_lo:[0,1] neg_hi:[0,1]
	v_pk_add_f32 v[28:29], v[28:29], v[0:1] op_sel_hi:[1,0] neg_lo:[0,1] neg_hi:[0,1]
	v_pk_add_f32 v[12:13], v[12:13], v[0:1] op_sel_hi:[1,0] neg_lo:[0,1] neg_hi:[0,1]
	v_pk_add_f32 v[30:31], v[30:31], v[0:1] op_sel_hi:[1,0] neg_lo:[0,1] neg_hi:[0,1]
	v_pk_add_f32 v[14:15], v[14:15], v[0:1] op_sel_hi:[1,0] neg_lo:[0,1] neg_hi:[0,1]
	v_pk_add_f32 v[32:33], v[32:33], v[0:1] op_sel_hi:[1,0] neg_lo:[0,1] neg_hi:[0,1]
	v_pk_add_f32 v[16:17], v[16:17], v[0:1] op_sel_hi:[1,0] neg_lo:[0,1] neg_hi:[0,1]
	s_setprio 1
	v_exp_f32_e32 v19, v2
	v_exp_f32_e32 v20, v3
	v_exp_f32_e32 v21, v4
	ds_read_b128 v[2:5], v213 offset:12288
	ds_read_b128 v[36:39], v213 offset:12800
	v_exp_f32_e32 v18, v18
	s_nop 0
	v_exp_f32_e32 v22, v22
	v_exp_f32_e32 v23, v23
	v_exp_f32_e32 v24, v24
	v_exp_f32_e32 v25, v25
	s_waitcnt lgkmcnt(1)
	v_mfma_f32_32x32x16_bf16 v[98:113], v[2:5], v[196:199], v[82:97]
	ds_read_b128 v[40:43], v213 offset:14336
	ds_read_b128 v[44:47], v213 offset:14848
	v_exp_f32_e32 v26, v26
	v_exp_f32_e32 v27, v27
	v_exp_f32_e32 v28, v28
	v_exp_f32_e32 v29, v29
	s_waitcnt lgkmcnt(2)
	v_mfma_f32_32x32x16_bf16 v[114:129], v[36:39], v[196:199], v[82:97]
	v_exp_f32_e32 v30, v30
	v_exp_f32_e32 v31, v31
	v_exp_f32_e32 v32, v32
	v_exp_f32_e32 v33, v33
	s_nop 0
	v_add_f32_e32 v2, 0, v18
	v_add_f32_e32 v2, v19, v2
	v_add_f32_e32 v2, v20, v2
	v_add_f32_e32 v52, v21, v2
	s_waitcnt lgkmcnt(1)
	v_mfma_f32_32x32x16_bf16 v[98:113], v[40:43], v[192:195], v[98:113]
	v_exp_f32_e32 v2, v48
	v_exp_f32_e32 v3, v49
	v_exp_f32_e32 v4, v50
	v_exp_f32_e32 v5, v51
	ds_read_b128 v[36:39], v213 offset:16384
	ds_read_b128 v[48:51], v213 offset:16896
	v_add_f32_e32 v40, v52, v22
	v_add_f32_e32 v40, v23, v40
	v_add_f32_e32 v40, v24, v40
	v_add_f32_e32 v40, v25, v40
	s_waitcnt lgkmcnt(2)
	v_mfma_f32_32x32x16_bf16 v[114:129], v[44:47], v[192:195], v[114:129]
	v_add_f32_e32 v40, v26, v40
	v_add_f32_e32 v40, v27, v40
	v_add_f32_e32 v40, v28, v40
	v_exp_f32_e32 v6, v6
	v_exp_f32_e32 v7, v7
	v_exp_f32_e32 v8, v8
	v_exp_f32_e32 v9, v9
	v_add_f32_e32 v44, v29, v40
	v_cvt_pk_bf16_f32 v160, v18, v19
	v_cvt_pk_bf16_f32 v161, v20, v21
	s_waitcnt lgkmcnt(1)
	v_mfma_f32_32x32x16_bf16 v[98:113], v[36:39], v[188:191], v[98:113]
	ds_read_b128 v[18:21], v213 offset:18432
	ds_read_b128 v[40:43], v213 offset:18944
	v_add_f32_e32 v36, v30, v44
	v_add_f32_e32 v36, v31, v36
	v_add_f32_e32 v36, v32, v36
	v_exp_f32_e32 v10, v10
	v_exp_f32_e32 v11, v11
	v_exp_f32_e32 v12, v12
	v_exp_f32_e32 v13, v13
	v_add_f32_e32 v36, v33, v36
	v_cvt_pk_bf16_f32 v162, v22, v23
	v_cvt_pk_bf16_f32 v163, v24, v25
	s_waitcnt lgkmcnt(2)
	v_mfma_f32_32x32x16_bf16 v[114:129], v[48:51], v[188:191], v[114:129]
	v_exp_f32_e32 v14, v14
	v_exp_f32_e32 v15, v15
	v_exp_f32_e32 v16, v16
	v_exp_f32_e32 v17, v17
	v_cvt_pk_bf16_f32 v164, v26, v27
	v_add_f32_e32 v22, v36, v2
	v_add_f32_e32 v22, v3, v22
	v_add_f32_e32 v22, v4, v22
	v_add_f32_e32 v36, v5, v22
	v_cvt_pk_bf16_f32 v165, v28, v29
	s_waitcnt lgkmcnt(1)
	v_mfma_f32_32x32x16_bf16 v[98:113], v[18:21], v[184:187], v[98:113]
	ds_read_b128 v[22:25], v213 offset:20480
	ds_read_b128 v[26:29], v213 offset:20992
	v_add_f32_e32 v36, v36, v6
	v_add_f32_e32 v36, v7, v36
	v_add_f32_e32 v36, v8, v36
	v_add_f32_e32 v36, v9, v36
	v_cvt_pk_bf16_f32 v166, v30, v31
	v_cvt_pk_bf16_f32 v167, v32, v33
	s_waitcnt lgkmcnt(2)
	v_mfma_f32_32x32x16_bf16 v[114:129], v[40:43], v[184:187], v[114:129]
	v_add_f32_e32 v18, v10, v36
	v_add_f32_e32 v18, v11, v18
	v_add_f32_e32 v18, v12, v18
	v_add_f32_e32 v36, v13, v18
	v_cvt_pk_bf16_f32 v168, v2, v3
	v_cvt_pk_bf16_f32 v169, v4, v5
	s_waitcnt lgkmcnt(1)
	v_mfma_f32_32x32x16_bf16 v[98:113], v[22:25], v[180:183], v[98:113]
	ds_read_b128 v[18:21], v213 offset:22528
	ds_read_b128 v[30:33], v213 offset:23040
	v_add_f32_e32 v2, v14, v36
	v_add_f32_e32 v2, v15, v2
	v_add_f32_e32 v2, v16, v2
	v_add_f32_e32 v2, v17, v2
	v_cvt_pk_bf16_f32 v170, v6, v7
	v_cvt_pk_bf16_f32 v171, v8, v9
	s_waitcnt lgkmcnt(2)
	v_mfma_f32_32x32x16_bf16 v[114:129], v[26:29], v[180:183], v[114:129]
	v_cvt_pk_bf16_f32 v172, v10, v11
	v_cvt_pk_bf16_f32 v173, v12, v13
	s_waitcnt lgkmcnt(1)
	v_mfma_f32_32x32x16_bf16 v[98:113], v[18:21], v[176:179], v[98:113]
	v_cvt_pk_bf16_f32 v174, v14, v15
	v_cvt_pk_bf16_f32 v175, v16, v17
	s_waitcnt lgkmcnt(0)
	v_mfma_f32_32x32x16_bf16 v[114:129], v[30:33], v[176:179], v[114:129]
	s_setprio 0
	v_lshl_add_u64 v[4:5], v[204:205], 0, s[22:23]
	s_mov_b32 s0, m0
	s_mov_b32 m0, s44
	s_nop 0
	global_load_lds_dwordx4 v[4:5], off
	s_mov_b32 m0, s0
	s_and_saveexec_b64 s[0:1], s[2:3]
	s_cbranch_execz .LBB0_1154
	v_lshl_add_u64 v[4:5], v[202:203], 0, s[26:27]
	s_mov_b32 s43, m0
	s_mov_b32 m0, s70
	s_nop 0
	global_load_lds_dwordx4 v[4:5], off
	s_mov_b32 m0, s43

; __device__ __forceinline__ int crow(int r, int hi) { return (r & 3) + 8 * (r >> 2) + 4 * hi; }
; #define MLA_WAIT_BAR(N) asm volatile("s_waitcnt vmcnt(" #N ") lgkmcnt(0)\n\ts_barrier" ::: "memory")
; #define MLA_PVW(slot) pv(o, vb0 + (slot) * VSLOT, __builtin_bit_cast(bf16x8, pw0), __builtin_bit_cast(bf16x8, pw1), __builtin_bit_cast(bf16x8, pw2), __builtin_bit_cast(bf16x8, pw3))
; #define MLA_RESCB() do { if (resc) { asm volatile("s_waitcnt lgkmcnt(0)" ::: "memory"); _Pragma("unroll") for (int r = 0; r < 16; ++r) { const float g_ = wsf[crow(r, hi)]; o[0][r] *= g_; o[1][r] *= g_; } resc = false; } } while (0)
; template <int THRL, bool LATE> __device__ __forceinline__ void unit_stag(int b, int h, int qb, const unsigned short* Q, const unsigned short* KV, const unsigned short* KPE, unsigned short* O, char* shm, const int wave_) {
;     ...
;     MLA_WAIT_BAR(0);
;     if (LATE) { MLA_PVW((NT - 2) & 3); MLA_RESCB(); }
;     MLA_SOFT(pB0, pB1);
;     MLA_PVW((NT - 1) & 3);
;     { auto rr = __builtin_amdgcn_permlane32_swap(__float_as_uint(l_reg), __float_as_uint(l_reg), false, false); l_reg = __uint_as_float(rr[0]) + __uint_as_float(rr[1]); }
;     if (hi == 0) wsf[32 + r32] = l_reg; asm volatile("s_waitcnt lgkmcnt(0)" ::: "memory");
;     float rli[16];
; #pragma unroll
;     for (int r = 0; r < 16; ++r) rli[r] = __builtin_amdgcn_rcpf(wsf[32 + crow(r, hi)]);
.LBB0_1181:
	v_exp_f32_e32 v50, v50
	v_exp_f32_e32 v51, v51
	v_exp_f32_e32 v52, v52
	v_exp_f32_e32 v53, v53
	s_waitcnt vmcnt(0) lgkmcnt(0)
	s_barrier
	v_exp_f32_e32 v34, v34
	v_exp_f32_e32 v54, v54
	v_exp_f32_e32 v55, v55
	v_exp_f32_e32 v56, v56
	v_exp_f32_e32 v57, v57
	v_exp_f32_e32 v35, v35
	v_exp_f32_e32 v58, v58
	v_exp_f32_e32 v59, v59
	v_exp_f32_e32 v60, v60
	v_exp_f32_e32 v61, v61
	v_exp_f32_e32 v36, v36
	v_exp_f32_e32 v62, v62
	v_exp_f32_e32 v63, v63
	v_exp_f32_e32 v64, v64
	v_exp_f32_e32 v65, v65
	v_exp_f32_e32 v37, v37
	s_nop 0
	v_exp_f32_e32 v38, v38
	v_exp_f32_e32 v39, v39
	v_exp_f32_e32 v40, v40
	v_exp_f32_e32 v41, v41
	v_add_f32_e32 v0, 0, v50
	v_exp_f32_e32 v42, v42
	v_exp_f32_e32 v43, v43
	v_exp_f32_e32 v44, v44
	v_exp_f32_e32 v45, v45
	v_add_f32_e32 v0, v51, v0
	v_add_f32_e32 v0, v52, v0
	v_exp_f32_e32 v46, v46
	v_exp_f32_e32 v47, v47
	v_exp_f32_e32 v48, v48
	v_exp_f32_e32 v49, v49
	v_add_f32_e32 v0, v53, v0
	v_cvt_pk_bf16_f32 v160, v50, v51
	v_add_f32_e32 v0, v54, v0
	v_add_f32_e32 v0, v55, v0
	v_add_f32_e32 v0, v56, v0
	v_add_f32_e32 v0, v57, v0
	v_cvt_pk_bf16_f32 v161, v52, v53
	v_add_f32_e32 v0, v58, v0
	v_add_f32_e32 v0, v59, v0
	v_add_f32_e32 v0, v60, v0
	v_add_f32_e32 v0, v61, v0
	v_cvt_pk_bf16_f32 v164, v58, v59
	v_add_f32_e32 v0, v62, v0
	v_add_f32_e32 v0, v63, v0
	v_add_f32_e32 v0, v64, v0
	v_add_f32_e32 v0, v65, v0
	v_cvt_pk_bf16_f32 v165, v60, v61
	v_add_f32_e32 v0, v34, v0
	v_add_f32_e32 v0, v35, v0
	v_add_f32_e32 v0, v36, v0
	v_add_f32_e32 v0, v37, v0
	v_cvt_pk_bf16_f32 v168, v34, v35
	v_add_f32_e32 v0, v38, v0
	v_add_f32_e32 v0, v39, v0
	v_add_f32_e32 v0, v40, v0
	v_add_f32_e32 v0, v41, v0
	v_cvt_pk_bf16_f32 v169, v36, v37
	v_add_f32_e32 v0, v42, v0
	v_add_f32_e32 v0, v43, v0
	v_add_f32_e32 v0, v44, v0
	v_add_f32_e32 v0, v45, v0
	v_cvt_pk_bf16_f32 v172, v42, v43
	v_add_f32_e32 v0, v46, v0
	v_add_f32_e32 v0, v47, v0
	v_add_f32_e32 v0, v48, v0
	v_add_f32_e32 v0, v49, v0
	v_cvt_pk_bf16_f32 v173, v44, v45
	v_cvt_pk_bf16_f32 v162, v54, v55
	v_cvt_pk_bf16_f32 v163, v56, v57
	v_add_u32_e32 v54, 0x6000, v211
	v_cvt_pk_bf16_f32 v166, v62, v63
	v_cvt_pk_bf16_f32 v167, v64, v65
	v_add_f32_e32 v0, v98, v0
	v_cvt_pk_bf16_f32 v170, v38, v39
	v_cvt_pk_bf16_f32 v171, v40, v41
	s_nop 0
	v_cvt_pk_bf16_f32 v174, v46, v47
	v_cvt_pk_bf16_f32 v175, v48, v49
	ds_read_b64_tr_b16 v[34:35],v54 offset:0
	ds_read_b64_tr_b16 v[36:37],v54 offset:512
	ds_read_b64_tr_b16 v[38:39],v54 offset:1024
	ds_read_b64_tr_b16 v[40:41],v54 offset:1536
	ds_read_b64_tr_b16 v[42:43],v54 offset:2048
	ds_read_b64_tr_b16 v[44:45],v54 offset:2560
	ds_read_b64_tr_b16 v[46:47],v54 offset:3072
	ds_read_b64_tr_b16 v[48:49],v54 offset:3584
	s_waitcnt lgkmcnt(0)
	s_nop 0
	v_mfma_f32_32x32x16_bf16 v[2:17], v[160:163], v[34:37], v[2:17]
	ds_read_b64_tr_b16 v[34:35],v54 offset:4096
	ds_read_b64_tr_b16 v[36:37],v54 offset:4608
	v_mfma_f32_32x32x16_bf16 v[2:17], v[164:167], v[38:41], v[2:17]
	ds_read_b64_tr_b16 v[38:39],v54 offset:5120
	ds_read_b64_tr_b16 v[40:41],v54 offset:5632
	v_mfma_f32_32x32x16_bf16 v[2:17], v[168:171], v[42:45], v[2:17]
	ds_read_b64_tr_b16 v[42:43],v54 offset:6144
	ds_read_b64_tr_b16 v[44:45],v54 offset:6656
	ds_read_b64_tr_b16 v[50:51],v54 offset:7168
	ds_read_b64_tr_b16 v[52:53],v54 offset:7680
	s_waitcnt lgkmcnt(0)
	v_mfma_f32_32x32x16_bf16 v[2:17], v[172:175], v[46:49], v[2:17]
	v_mfma_f32_32x32x16_bf16 v[18:33], v[160:163], v[34:37], v[18:33]
	v_mov_b32_e32 v34, v0
	s_nop 1
	v_permlane32_swap_b32_e32 v0, v34
	v_mfma_f32_32x32x16_bf16 v[18:33], v[164:167], v[38:41], v[18:33]
	v_mfma_f32_32x32x16_bf16 v[18:33], v[168:171], v[42:45], v[18:33]
	v_mfma_f32_32x32x16_bf16 v[18:33], v[172:175], v[50:53], v[18:33]
	s_and_saveexec_b64 s[0:1], s[2:3]
	v_add_f32_e32 v0, v0, v34
	ds_write_b32 v120, v0 offset:128
	s_or_b64 exec, exec, s[0:1]
	s_waitcnt lgkmcnt(0)
	v_lshl_add_u32 v0, v129, 2, s69
	ds_read_b128 v[34:37], v0 offset:128
	ds_read_b128 v[38:41], v0 offset:160
	s_lshl_b32 s2, s68, 12
	s_add_i32 s2, s2, 0
	s_add_i32 s2, s2, 0x11800
	s_waitcnt lgkmcnt(1)
	v_rcp_f32_e32 v42, v34
	v_rcp_f32_e32 v43, v35
	v_rcp_f32_e32 v44, v36
	v_rcp_f32_e32 v45, v37
	s_waitcnt lgkmcnt(0)
	v_rcp_f32_e32 v46, v38
	ds_read_b128 v[34:37], v0 offset:192
	v_rcp_f32_e32 v47, v39
	v_rcp_f32_e32 v48, v40
	v_rcp_f32_e32 v49, v41
	ds_read_b128 v[38:41], v0 offset:224
	s_waitcnt lgkmcnt(1)
	v_rcp_f32_e32 v0, v34
	v_rcp_f32_e32 v34, v35
	v_rcp_f32_e32 v35, v36
	v_rcp_f32_e32 v36, v37
	s_waitcnt lgkmcnt(0)
; __device__ __forceinline__ void unit(int b, int h, int qb, const unsigned short* Q, const unsigned short* KV, const unsigned short* KPE, unsigned short* O, char* shm, const int wave_) {
;     int tid_ = tid_from_wave(wave_); asm volatile("" : "+v"(tid_));
;     const int tid = tid_, lane = tid & 63, r32 = lane & 31, hi = lane >> 5; const int wid = __builtin_amdgcn_readfirstlane(tid >> 6);
;     const long rowbase = (long)b * SEQ; const int q0 = qb * QB;
;     const unsigned short* Qw = Q + (rowbase + q0 + wid * QBLK) * QP + h * 96;
;     const unsigned short* Kh = KV + rowbase * KVP + h * 128; const unsigned short* Vh = Kh + 64; const unsigned short* Ph = KPE + rowbase * PEP;
;     const unsigned lds0 = (unsigned)(uintptr_t)shm;
;     __attribute__((address_space(3))) float* wsf = (__attribute__((address_space(3))) float*)((lds_cptr)shm + LDS_WS) + wid * 64;
;     const unsigned short* ksrc = Kh + (long)lane * KVP + wid * 8;
;     const unsigned short* psrc = Ph + (long)(32 * (wid & 1) + r32) * PEP + (wid >> 1) * 8;
;     const unsigned short* vsrc = Vh + (long)(16 * (wid & 3) + (lane >> 2)) * KVP + (wid >> 2) * 32 + (lane & 3) * 8;
;     const unsigned kdst = lds0 + LDS_K + wid * 1024, pdst = lds0 + LDS_K + (8 + (wid >> 1)) * 1024 + (wid & 1) * 512, vdst = lds0 + LDS_V + wid * 1024;
; template <int THRL, bool LATE> __device__ __forceinline__ void unit_stag(int b, int h, int qb, const unsigned short* Q, const unsigned short* KV, const unsigned short* KPE, unsigned short* O, char* shm, const int wave_) {
;     ...
;     unsigned short* Ow = O + (rowbase + q0 + wid * QBLK) * OP + 512 + h * 64;
;     { __attribute__((address_space(3))) unsigned short* stg = (__attribute__((address_space(3))) unsigned short*)((lds_cptr)shm + S4_OST) + wid * 2048;
; #pragma unroll
;       for (int r = 0; r < 16; ++r) { const int orow = crow(r, hi);
; #pragma unroll
;           for (int d0 = 0; d0 < 2; ++d0) stg[orow * 64 + d0 * 32 + r32] = (unsigned short)(cvtpk_s(o[d0][r] * rli[r], 0.f) & 0xffffu); }
;       asm volatile("s_waitcnt lgkmcnt(0)" ::: "memory");
; #pragma unroll
;       for (int i = 0; i < 4; ++i) { const int row = i * 8 + (lane >> 3), ch = lane & 7; const u32x4 v = *(const __attribute__((address_space(3))) u32x4*)(stg + row * 64 + ch * 8); *(u32x4*)(Ow + (long)row * OP + ch * 8) = v; } }
;     asm volatile("s_waitcnt vmcnt(0) lgkmcnt(0)\n\ts_barrier" ::: "memory");
	v_rcp_f32_e32 v37, v38
	v_rcp_f32_e32 v38, v39
	v_rcp_f32_e32 v39, v40
	v_rcp_f32_e32 v40, v41
	s_lshl_b64 s[0:1], s[40:41], 11
	v_lshl_add_u32 v41, v209, 1, s2
	v_mul_f32_e32 v2, v2, v42
	v_lshl_add_u32 v50, v210, 9, v41
	v_cvt_pk_bf16_f32 v2, v2, s0
	ds_write_b16 v50, v2
	v_mul_f32_e32 v2, v18, v42
	v_cvt_pk_bf16_f32 v2, v2, s0
	ds_write_b16 v50, v2 offset:64
	v_mul_f32_e32 v2, v3, v43
	v_cvt_pk_bf16_f32 v2, v2, s0
	ds_write_b16 v50, v2 offset:128
	v_mul_f32_e32 v2, v19, v43
	v_cvt_pk_bf16_f32 v2, v2, s0
	v_mul_f32_e32 v3, v4, v44
	ds_write_b16 v50, v2 offset:192
	v_lshl_add_u32 v2, v125, 7, v41
	v_cvt_pk_bf16_f32 v3, v3, s0
	ds_write_b16 v2, v3
	v_mul_f32_e32 v3, v20, v44
	v_cvt_pk_bf16_f32 v3, v3, s0
	ds_write_b16 v2, v3 offset:64
	v_mul_f32_e32 v3, v5, v45
	v_lshl_add_u32 v2, v126, 7, v41
	v_cvt_pk_bf16_f32 v3, v3, s0
	ds_write_b16 v2, v3
	v_mul_f32_e32 v3, v21, v45
	v_cvt_pk_bf16_f32 v3, v3, s0
	ds_write_b16 v2, v3 offset:64
	v_mul_f32_e32 v3, v6, v46
	v_lshl_add_u32 v2, v127, 7, v41
	v_cvt_pk_bf16_f32 v3, v3, s0
	ds_write_b16 v2, v3
	v_mul_f32_e32 v3, v22, v46
	v_cvt_pk_bf16_f32 v3, v3, s0
	ds_write_b16 v2, v3 offset:64
	v_mul_f32_e32 v3, v7, v47
	v_lshl_add_u32 v2, v128, 7, v41
	v_cvt_pk_bf16_f32 v3, v3, s0
	ds_write_b16 v2, v3
	v_mul_f32_e32 v3, v23, v47
	v_cvt_pk_bf16_f32 v3, v3, s0
	ds_write_b16 v2, v3 offset:64
	v_mul_f32_e32 v3, v8, v48
	v_lshl_add_u32 v2, v124, 7, v41
	v_cvt_pk_bf16_f32 v3, v3, s0
	ds_write_b16 v2, v3
	v_mul_f32_e32 v3, v24, v48
	v_cvt_pk_bf16_f32 v3, v3, s0
	ds_write_b16 v2, v3 offset:64
	v_mul_f32_e32 v3, v9, v49
	v_lshl_add_u32 v2, v123, 7, v41
	v_cvt_pk_bf16_f32 v3, v3, s0
	ds_write_b16 v2, v3
	v_mul_f32_e32 v3, v25, v49
	v_cvt_pk_bf16_f32 v3, v3, s0
	ds_write_b16 v2, v3 offset:64
	v_mul_f32_e32 v3, v10, v0
	v_mul_f32_e32 v0, v26, v0
	v_lshl_add_u32 v2, v122, 7, v41
	v_cvt_pk_bf16_f32 v3, v3, s0
	v_cvt_pk_bf16_f32 v0, v0, s0
	ds_write_b16 v2, v3
	ds_write_b16 v2, v0 offset:64
	v_mul_f32_e32 v2, v11, v34
	v_lshl_add_u32 v0, v121, 7, v41
	v_cvt_pk_bf16_f32 v2, v2, s0
	ds_write_b16 v0, v2
	v_mul_f32_e32 v2, v27, v34
	v_cvt_pk_bf16_f32 v2, v2, s0
	ds_write_b16 v0, v2 offset:64
	v_mul_f32_e32 v2, v12, v35
	v_lshl_add_u32 v0, v119, 7, v41
	v_cvt_pk_bf16_f32 v2, v2, s0
	ds_write_b16 v0, v2
	v_mul_f32_e32 v2, v28, v35
	v_cvt_pk_bf16_f32 v2, v2, s0
	ds_write_b16 v0, v2 offset:64
	v_mul_f32_e32 v2, v13, v36
	v_lshl_add_u32 v0, v118, 7, v41
	v_cvt_pk_bf16_f32 v2, v2, s0
	ds_write_b16 v0, v2
	v_mul_f32_e32 v2, v29, v36
	v_cvt_pk_bf16_f32 v2, v2, s0
	ds_write_b16 v0, v2 offset:64
	v_mul_f32_e32 v2, v14, v37
	v_lshl_add_u32 v0, v117, 7, v41
	v_cvt_pk_bf16_f32 v2, v2, s0
	ds_write_b16 v0, v2
	v_mul_f32_e32 v2, v30, v37
	v_cvt_pk_bf16_f32 v2, v2, s0
	ds_write_b16 v0, v2 offset:64
	v_mul_f32_e32 v2, v15, v38
	v_lshl_add_u32 v0, v116, 7, v41
	v_cvt_pk_bf16_f32 v2, v2, s0
	ds_write_b16 v0, v2
	v_mul_f32_e32 v2, v31, v38
	v_cvt_pk_bf16_f32 v2, v2, s0
	ds_write_b16 v0, v2 offset:64
	v_mul_f32_e32 v2, v16, v39
	v_lshl_add_u32 v0, v115, 7, v41
	v_cvt_pk_bf16_f32 v2, v2, s0
	ds_write_b16 v0, v2
	v_mul_f32_e32 v2, v32, v39
	v_cvt_pk_bf16_f32 v2, v2, s0
	ds_write_b16 v0, v2 offset:64
	v_mul_f32_e32 v2, v17, v40
	v_lshl_add_u32 v0, v114, 7, v41
	v_cvt_pk_bf16_f32 v2, v2, s0
	ds_write_b16 v0, v2
	v_mul_f32_e32 v2, v33, v40
	v_cvt_pk_bf16_f32 v2, v2, s0
	ds_write_b16 v0, v2 offset:64
	v_lshlrev_b32_e32 v0, 1, v208
	s_add_u32 s0, s65, s0
	v_and_b32_e32 v0, 0x70, v0
	s_addc_u32 s1, s66, s1
	v_lshrrev_b32_e32 v14, 3, v207
	v_add_u32_e32 v15, s2, v0
	s_waitcnt lgkmcnt(0)
	v_lshl_add_u64 v[10:11], s[0:1], 0, v[0:1]
	v_lshl_add_u32 v0, v14, 7, v15
	v_or_b32_e32 v16, 8, v14
	ds_read_b128 v[2:5], v0
	v_lshl_add_u32 v6, v16, 7, v15
	ds_read_b128 v[6:9], v6
	v_lshlrev_b32_e32 v0, 11, v14
	v_lshl_add_u64 v[12:13], v[10:11], 0, v[0:1]
	v_lshlrev_b32_e32 v0, 11, v16
	s_waitcnt lgkmcnt(1)
	global_store_dwordx4 v[12:13], v[2:5], off offset:1024
	s_nop 1
	v_lshl_add_u64 v[2:3], v[10:11], 0, v[0:1]
	v_or_b32_e32 v0, 16, v14
	s_waitcnt lgkmcnt(0)
	global_store_dwordx4 v[2:3], v[6:9], off offset:1024
	v_lshl_add_u32 v2, v0, 7, v15
	v_or_b32_e32 v14, 24, v14
	ds_read_b128 v[2:5], v2
	v_lshl_add_u32 v6, v14, 7, v15
	ds_read_b128 v[6:9], v6
	v_lshlrev_b32_e32 v0, 11, v0
	v_lshl_add_u64 v[12:13], v[10:11], 0, v[0:1]
	v_lshlrev_b32_e32 v0, 11, v14
	s_waitcnt lgkmcnt(1)
	global_store_dwordx4 v[12:13], v[2:5], off offset:1024
	s_nop 1
	v_lshl_add_u64 v[2:3], v[10:11], 0, v[0:1]
	s_waitcnt lgkmcnt(0)
	global_store_dwordx4 v[2:3], v[6:9], off offset:1024
	s_waitcnt lgkmcnt(0)
	s_barrier
	s_cbranch_execnz .LBB0_1087
.LBB0_1184:
	v_mbcnt_lo_u32_b32 v0, -1, 0
	v_mbcnt_hi_u32_b32 v0, -1, v0
	s_nop 0
	v_add_u32_e32 v8, s96, v0
	s_nop 0
	v_readfirstlane_b32 s45, v8
	s_ashr_i32 s10, s45, 6
	s_lshl_b32 s47, s10, 5
	s_ashr_i32 s1, s47, 31
	s_add_u32 s0, s34, s47
	s_addc_u32 s1, s35, s1
	v_and_b32_e32 v98, 31, v8
	s_mul_i32 s2, s1, 0x600
	s_mul_hi_u32 s3, s0, 0x600
	s_add_i32 s3, s3, s2
	s_mul_i32 s2, s0, 0x600
	v_mul_u32_u24_e32 v0, 0x300, v98
	v_bfe_u32 v99, v8, 5, 1
	s_add_u32 s2, s63, s2
	v_lshlrev_b32_e32 v0, 1, v0
	s_addc_u32 s3, s64, s3
	v_lshl_or_b32 v0, v99, 4, v0
	global_load_dwordx4 v[66:69], v0, s[2:3]
	global_load_dwordx4 v[70:73], v0, s[2:3] offset:32
	global_load_dwordx4 v[74:77], v0, s[2:3] offset:64
	global_load_dwordx4 v[78:81], v0, s[2:3] offset:96
	global_load_dwordx4 v[82:85], v0, s[2:3] offset:128
	global_load_dwordx4 v[86:89], v0, s[2:3] offset:160
	s_ashr_i32 s42, s45, 7
	s_lshl_b32 s2, s10, 3
	s_lshl_b32 s40, s42, 3
	v_and_b32_e32 v96, 63, v8
	s_ashr_i32 s3, s2, 31
	s_and_b32 s43, s10, 1
	s_ashr_i32 s41, s40, 31
	s_lshl_b32 s68, s10, 10
	s_lshl_b32 s42, s42, 10
	s_cmp_lg_u32 0, -1
	v_lshlrev_b32_e32 v0, 11, v96
	s_cselect_b32 s44, 0, 0
	v_lshl_add_u64 v[2:3], s[36:37], 0, v[0:1]
	v_lshlrev_b32_e32 v0, 6, v98
	s_add_i32 s42, s44, s42
	s_lshl_b32 s46, s43, 9
	v_lshl_add_u64 v[2:3], s[2:3], 1, v[2:3]
	v_lshl_or_b32 v0, s43, 11, v0
	s_add_i32 s43, s68, s44
	s_mov_b32 s2, m0
	s_mov_b32 m0, s43
	s_nop 0
	global_load_lds_dwordx4 v[2:3], off
	s_mov_b32 m0, s2
	s_add_i32 s42, s42, s46
	v_lshl_add_u64 v[4:5], s[38:39], 0, v[0:1]
	s_addk_i32 s42, 0x2000
	v_lshl_add_u64 v[4:5], s[40:41], 1, v[4:5]
	v_cmp_gt_u32_e64 s[2:3], 32, v96
	s_and_saveexec_b64 s[40:41], s[2:3]
	s_cbranch_execz .LBB0_1186
	s_mov_b32 s44, m0
	s_mov_b32 m0, s42
	s_nop 0
	global_load_lds_dwordx4 v[4:5], off
	s_mov_b32 m0, s44

; __device__ __forceinline__ int crow(int r, int hi) { return (r & 3) + 8 * (r >> 2) + 4 * hi; }
; __device__ __forceinline__ float max3f(float a, float b, float c) { float r; asm("v_max3_f32 %0, %1, %2, %3" : "=v"(r) : "v"(a), "v"(b), "v"(c)); return r; }
; __device__ __forceinline__ void cmask(f32x16& p0, f32x16& p1, int jb, int qrel, int hi) {
;     const float NEG = -INFINITY; const int kb = 64 * jb + 4 * hi;
; #pragma unroll
;     for (int r = 0; r < 16; ++r) { const int kv = kb + (r & 3) + 8 * (r >> 2); if (kv > qrel) p0[r] = NEG; if (kv + 32 > qrel) p1[r] = NEG; }
; }
; __device__ __forceinline__ float rowmax(const f32x16& p0, const f32x16& p1) {
;     float a = max3f(p0[0], p0[1], p1[0]), b = max3f(p0[2], p0[3], p1[1]); a = max3f(a, p1[2], p1[3]);
; #pragma unroll
;     for (int r = 4; r < 16; r += 4) { a = max3f(a, p0[r], p0[r + 1]); b = max3f(b, p0[r + 2], p0[r + 3]); a = max3f(a, p1[r], p1[r + 1]); b = max3f(b, p1[r + 2], p1[r + 3]); }
;     const float m = fmaxf(a, b);
;     auto rr = __builtin_amdgcn_permlane32_swap(__float_as_uint(m), __float_as_uint(m), false, false);
;     return fmaxf(__uint_as_float(rr[0]), __uint_as_float(rr[1]));
; }
; __device__ __forceinline__ void unit(int b, int h, int qb, const unsigned short* Q, const unsigned short* KV, const unsigned short* KPE, unsigned short* O, char* shm, const int wave_) {
;     ...
;         { const lds_cptr kp = kp0 + slot * KSLOT;
; #pragma unroll
;           for (int d0 = 0; d0 < 6; ++d0) { const bf16x8 b0 = *(const __attribute__((address_space(3))) bf16x8*)(kp + d0 * 2048), b1 = *(const __attribute__((address_space(3))) bf16x8*)(kp + d0 * 2048 + 512);
;               p0 = __builtin_amdgcn_mfma_f32_32x32x16_bf16(b0, qr[d0], p0, 0, 0, 0); p1 = __builtin_amdgcn_mfma_f32_32x32x16_bf16(b1, qr[d0], p1, 0, 0, 0); } }
;         { const int jb = t - (NT - 4); if (jb >= 0) cmask(p0, p1, jb, qrel, hi); }
;         const float rm = rowmax(p0, p1), mn = fmaxf(m, rm);
;         if (__any(mn > m)) {
;             const float al = __builtin_amdgcn_exp2f(m - mn); l *= al; m = mn;
;             if (hi == 0) wsf[r32] = al;
;             asm volatile("s_waitcnt lgkmcnt(0)" ::: "memory");
; #pragma unroll
;             for (int r = 0; r < 16; ++r) { const float f = wsf[crow(r, hi)]; o[0][r] *= f; o[1][r] *= f; }
;         }
.LBB0_1197:
	s_mul_i32 s40, s47, 0x3000
	v_add_u32_e32 v0, s40, v102
	ds_read_b128 v[34:37], v0
	ds_read_b128 v[38:41], v0 offset:512
	ds_read_b128 v[108:111], v0 offset:2048
	ds_read_b128 v[112:115], v0 offset:2560
	s_waitcnt vmcnt(5) lgkmcnt(3)
	v_mfma_f32_32x32x16_bf16 v[50:65], v[34:37], v[66:69], 0
	s_waitcnt lgkmcnt(2)
	v_mfma_f32_32x32x16_bf16 v[34:49], v[38:41], v[66:69], 0
	s_waitcnt vmcnt(4) lgkmcnt(1)
	v_mfma_f32_32x32x16_bf16 v[50:65], v[108:111], v[70:73], v[50:65]
	s_waitcnt lgkmcnt(0)
	v_mfma_f32_32x32x16_bf16 v[34:49], v[112:115], v[70:73], v[34:49]
	ds_read_b128 v[108:111], v0 offset:4096
	ds_read_b128 v[112:115], v0 offset:4608
	s_waitcnt vmcnt(3) lgkmcnt(1)
	v_mfma_f32_32x32x16_bf16 v[50:65], v[108:111], v[74:77], v[50:65]
	s_waitcnt lgkmcnt(0)
	v_mfma_f32_32x32x16_bf16 v[34:49], v[112:115], v[74:77], v[34:49]
	ds_read_b128 v[108:111], v0 offset:6144
	ds_read_b128 v[112:115], v0 offset:6656
	s_waitcnt vmcnt(2) lgkmcnt(1)
	v_mfma_f32_32x32x16_bf16 v[50:65], v[108:111], v[78:81], v[50:65]
	s_waitcnt lgkmcnt(0)
	v_mfma_f32_32x32x16_bf16 v[34:49], v[112:115], v[78:81], v[34:49]
	ds_read_b128 v[108:111], v0 offset:8192
	ds_read_b128 v[112:115], v0 offset:8704
	s_waitcnt vmcnt(1) lgkmcnt(1)
	v_mfma_f32_32x32x16_bf16 v[50:65], v[108:111], v[82:85], v[50:65]
	ds_read_b128 v[108:111], v0 offset:10752
	s_waitcnt lgkmcnt(1)
	v_mfma_f32_32x32x16_bf16 v[34:49], v[112:115], v[82:85], v[34:49]
	s_waitcnt lgkmcnt(0)
	v_mfma_f32_32x32x16_bf16 v[34:49], v[108:111], v[86:89], v[34:49]
	ds_read_b128 v[108:111], v0 offset:10240
	v_add_u32_e32 v0, s46, v104
	v_add_u32_e32 v107, 32, v0
	v_cmp_le_i32_e32 vcc, v107, v103
	s_waitcnt lgkmcnt(0)
	v_mfma_f32_32x32x16_bf16 v[50:65], v[108:111], v[86:89], v[50:65]
	s_nop 5
	v_cndmask_b32_e32 v112, v206, v34, vcc
	v_cmp_le_i32_e32 vcc, v0, v103
	v_add_u32_e32 v34, 33, v0
	s_nop 2
	v_cndmask_b32_e32 v118, v206, v50, vcc
	v_cmp_lt_i32_e32 vcc, v0, v103
	s_nop 1
	v_cndmask_b32_e32 v115, v206, v51, vcc
	v_cmp_le_i32_e32 vcc, v34, v103
	v_add_u32_e32 v34, 2, v0
	s_nop 0
	v_cndmask_b32_e32 v116, v206, v35, vcc
	v_cmp_le_i32_e32 vcc, v34, v103
	v_add_u32_e32 v34, 34, v0
	v_add_u32_e32 v35, 58, v0
	v_cndmask_b32_e32 v114, v206, v52, vcc
	v_cmp_le_i32_e32 vcc, v34, v103
	v_add_u32_e32 v34, 3, v0
	s_nop 0
	v_cndmask_b32_e32 v117, v206, v36, vcc
	v_cmp_le_i32_e32 vcc, v34, v103
	v_add_u32_e32 v34, 35, v0
	s_nop 0
	v_cndmask_b32_e32 v107, v206, v53, vcc
	v_cmp_le_i32_e32 vcc, v34, v103
	v_add_u32_e32 v34, 8, v0
	s_nop 0
	v_cndmask_b32_e32 v109, v206, v37, vcc
	v_cmp_le_i32_e32 vcc, v34, v103
	v_add_u32_e32 v34, 40, v0
	s_nop 0
	v_cndmask_b32_e32 v108, v206, v54, vcc
	v_cmp_le_i32_e32 vcc, v34, v103
	v_add_u32_e32 v34, 9, v0
	s_nop 0
	v_cndmask_b32_e32 v111, v206, v38, vcc
	v_cmp_le_i32_e32 vcc, v34, v103
	v_add_u32_e32 v34, 41, v0
	s_nop 0
	v_cndmask_b32_e32 v110, v206, v55, vcc
	v_cmp_le_i32_e32 vcc, v34, v103
	v_add_u32_e32 v34, 10, v0
	s_nop 0
	v_cndmask_b32_e32 v113, v206, v39, vcc
	v_cmp_le_i32_e32 vcc, v34, v103
	v_add_u32_e32 v34, 42, v0
	s_nop 0
	v_cndmask_b32_e32 v54, v206, v56, vcc
	v_cmp_le_i32_e32 vcc, v34, v103
	v_add_u32_e32 v34, 11, v0
	s_nop 0
	v_cndmask_b32_e32 v56, v206, v40, vcc
	v_cmp_le_i32_e32 vcc, v34, v103
	v_add_u32_e32 v34, 43, v0
	s_nop 0
	v_cndmask_b32_e32 v55, v206, v57, vcc
	v_cmp_le_i32_e32 vcc, v34, v103
	v_add_u32_e32 v34, 16, v0
	s_nop 0
	v_cndmask_b32_e32 v57, v206, v41, vcc
	v_cmp_le_i32_e32 vcc, v34, v103
	v_add_u32_e32 v34, 48, v0
	s_nop 0
	v_cndmask_b32_e32 v50, v206, v58, vcc
	v_cmp_le_i32_e32 vcc, v34, v103
	v_add_u32_e32 v34, 17, v0
	s_nop 0
	v_cndmask_b32_e32 v52, v206, v42, vcc
	v_cmp_le_i32_e32 vcc, v34, v103
	v_add_u32_e32 v34, 49, v0
	s_nop 0
	v_cndmask_b32_e32 v51, v206, v59, vcc
	v_cmp_le_i32_e32 vcc, v34, v103
	v_add_u32_e32 v34, 18, v0
	s_nop 0
	v_cndmask_b32_e32 v53, v206, v43, vcc
	v_cmp_le_i32_e32 vcc, v34, v103
	v_add_u32_e32 v34, 50, v0
	s_nop 0
	v_cndmask_b32_e32 v42, v206, v60, vcc
	v_cmp_le_i32_e32 vcc, v34, v103
	v_add_u32_e32 v34, 19, v0
	s_nop 0
	v_cndmask_b32_e32 v44, v206, v44, vcc
	v_cmp_le_i32_e32 vcc, v34, v103
	v_add_u32_e32 v34, 51, v0
	s_nop 0
	v_cndmask_b32_e32 v43, v206, v61, vcc
	v_cmp_le_i32_e32 vcc, v34, v103
	v_add_u32_e32 v34, 24, v0
	s_nop 0
	v_cndmask_b32_e32 v45, v206, v45, vcc
	v_cmp_le_i32_e32 vcc, v34, v103
	v_add_u32_e32 v34, 56, v0
	s_nop 0
	v_cndmask_b32_e32 v38, v206, v62, vcc
	v_cmp_le_i32_e32 vcc, v34, v103
	v_add_u32_e32 v34, 25, v0
	s_nop 0
	v_cndmask_b32_e32 v40, v206, v46, vcc
	v_cmp_le_i32_e32 vcc, v34, v103
	v_add_u32_e32 v34, 57, v0
	v_max3_f32 v46, v114, v107, v116
	s_nop 0
	v_cndmask_b32_e32 v39, v206, v63, vcc
	v_cmp_le_i32_e32 vcc, v34, v103
	v_add_u32_e32 v34, 26, v0
	v_max3_f32 v46, v46, v54, v55
	s_nop 0
	v_cndmask_b32_e32 v41, v206, v47, vcc
	v_cmp_le_i32_e32 vcc, v34, v103
	v_max3_f32 v46, v46, v56, v57
	s_nop 0
	v_max3_f32 v46, v46, v42, v43
	s_nop 0
	v_cndmask_b32_e32 v34, v206, v64, vcc
	v_cmp_le_i32_e32 vcc, v35, v103
	v_add_u32_e32 v35, 27, v0
	v_add_u32_e32 v0, 59, v0
	v_cndmask_b32_e32 v36, v206, v48, vcc
	v_cmp_le_i32_e32 vcc, v35, v103
	v_max3_f32 v46, v46, v44, v45
	s_nop 1
	v_cndmask_b32_e32 v35, v206, v65, vcc
	v_cmp_le_i32_e32 vcc, v0, v103
	v_max3_f32 v0, v118, v115, v112
	v_max3_f32 v46, v46, v34, v35
	s_nop 0
	v_max3_f32 v0, v0, v117, v109
	s_nop 0
	v_max3_f32 v0, v0, v108, v110
	v_cndmask_b32_e32 v37, v206, v49, vcc
	v_max3_f32 v0, v0, v111, v113
	v_max3_f32 v46, v46, v36, v37
	s_nop 0
	v_max3_f32 v0, v0, v50, v51
	v_max_f32_e32 v46, v46, v46
	v_max3_f32 v0, v0, v52, v53
	s_nop 0
	v_max3_f32 v0, v0, v38, v39
	s_nop 0
	v_max3_f32 v0, v0, v40, v41
	s_nop 0
	v_max_f32_e32 v0, v0, v0
	v_max_f32_e32 v0, v0, v46
	v_mov_b32_e32 v46, v0
	s_nop 1
	v_permlane32_swap_b32_e32 v0, v46
	v_max3_f32 v0, v119, v0, v46
	v_cmp_gt_f32_e32 vcc, v0, v119
	s_cbranch_vccz .LBB0_1201
	v_sub_f32_e32 v46, v119, v0
	v_exp_f32_e32 v46, v46
	s_and_saveexec_b64 s[40:41], s[2:3]
	ds_write_b32 v101, v46 offset:61440
	s_or_b64 exec, exec, s[40:41]
	s_waitcnt lgkmcnt(0)
	ds_read_b128 v[58:61], v100 offset:61536
	ds_read_b128 v[62:65], v100 offset:61504
	ds_read_b128 v[120:123], v100 offset:61472
	ds_read_b128 v[124:127], v100 offset:61440
	v_mul_f32_e32 v106, v106, v46
	s_waitcnt lgkmcnt(3)
	v_pk_mul_f32 v[32:33], v[32:33], v[60:61]
	s_waitcnt lgkmcnt(2)
	v_pk_mul_f32 v[28:29], v[28:29], v[64:65]
	s_waitcnt lgkmcnt(1)
	v_pk_mul_f32 v[24:25], v[24:25], v[122:123]
	s_waitcnt lgkmcnt(0)
	v_pk_mul_f32 v[20:21], v[20:21], v[126:127]
	v_pk_mul_f32 v[30:31], v[30:31], v[58:59]
	v_pk_mul_f32 v[26:27], v[26:27], v[62:63]
	v_pk_mul_f32 v[22:23], v[22:23], v[120:121]
	v_pk_mul_f32 v[18:19], v[18:19], v[124:125]
	v_pk_mul_f32 v[16:17], v[16:17], v[60:61]
	v_pk_mul_f32 v[12:13], v[12:13], v[64:65]
	v_pk_mul_f32 v[8:9], v[8:9], v[122:123]
	v_pk_mul_f32 v[4:5], v[4:5], v[126:127]
	v_pk_mul_f32 v[14:15], v[14:15], v[58:59]
	v_pk_mul_f32 v[10:11], v[10:11], v[62:63]
	v_pk_mul_f32 v[6:7], v[6:7], v[120:121]
	v_pk_mul_f32 v[2:3], v[2:3], v[124:125]
	s_branch .LBB0_1202

;     __device__ __forceinline__ bool next(int i, Unit& u) const {
;         int pl, n;
;         if (NT == 28 && G == 256 && l0 == 0) {
;             const int per = (nunits + 7) >> 3, x = c >> 5, j = c & 31, s = 32 * i + j; if (s >= per) return false;
;             const int L = x * per + s; if (L >= nunits) return false;
;             constexpr int PG = MOE_PG;
;             const int P = nunits / 28, full = (P / PG) * (PG * 28);
;             constexpr int NC = MOE_NC, NQ = 28 / NC;
;             if (L < full) { const int t = L / (NC * PG), r = L - t * (NC * PG), g = t / NQ, q = t - g * NQ; pl = PG * g + (r % PG); n = NC * q + (r / PG); }
;             else { const int L2 = L - full; pl = (P / PG) * PG + L2 / 28; n = L2 % 28; }
;         } else {
;         const int L = l0 + i * G + c; if (L >= nunits) return false;
;         pl = L / NT; n = L - pl * NT; }
;         const int p = p0 + pl;
;         const int e = __builtin_amdgcn_readfirstlane(pexp[p]);
;         u.pm = A_REL ? pl : p; u.po = A_REL ? p : pl; u.pn = n; u.pb = e * NT + n; return true;
.LBB0_1537:
	s_mov_b64 s[24:25], 0
	s_and_b64 vcc, exec, s[22:23]
	s_cbranch_vccz .LBB0_1539
	s_ashr_i32 s21, s20, 31
	s_lshl_b64 s[16:17], s[20:21], 2
	s_add_u32 s16, s62, s16
	s_addc_u32 s17, s63, s17
	s_load_dword s16, s[16:17], 0x0
	s_mov_b64 s[24:25], -1
	s_mov_b32 s18, s20
	s_waitcnt lgkmcnt(0)
	s_mul_i32 s16, s16, 28
	s_add_i32 s16, s16, s67

;     __device__ __forceinline__ bool next(int i, Unit& u) const {
;         int pl, n;
;         if (NT == 28 && G == 256 && l0 == 0) {
;             const int per = (nunits + 7) >> 3, x = c >> 5, j = c & 31, s = 32 * i + j; if (s >= per) return false;
;             const int L = x * per + s; if (L >= nunits) return false;
;             constexpr int PG = MOE_PG;
;             const int P = nunits / 28, full = (P / PG) * (PG * 28);
;             constexpr int NC = MOE_NC, NQ = 28 / NC;
;             if (L < full) { const int t = L / (NC * PG), r = L - t * (NC * PG), g = t / NQ, q = t - g * NQ; pl = PG * g + (r % PG); n = NC * q + (r / PG); }
;             else { const int L2 = L - full; pl = (P / PG) * PG + L2 / 28; n = L2 % 28; }
;         } else {
;         const int L = l0 + i * G + c; if (L >= nunits) return false;
;         pl = L / NT; n = L - pl * NT; }
;         const int p = p0 + pl;
;         const int e = __builtin_amdgcn_readfirstlane(pexp[p]);
;         u.pm = A_REL ? pl : p; u.po = A_REL ? p : pl; u.pn = n; u.pb = e * NT + n; return true;
.LBB0_1614:
	s_add_i32 s48, s48, 1
	s_mul_i32 s2, s48, s13
	s_add_i32 s2, s2, s40
	s_cmp_lt_i32 s2, s41
	s_cselect_b64 s[24:25], -1, 0
	s_cmp_ge_i32 s2, s41
	s_cbranch_scc1 .LBB0_1616
	s_ashr_i32 s3, s2, 31
	s_lshr_b32 s3, s3, 30
	s_add_i32 s3, s2, s3
	s_ashr_i32 s22, s3, 2
	s_and_b32 s3, s3, -4
	s_ashr_i32 s23, s22, 31
	s_sub_i32 s67, s2, s3
	s_lshl_b64 s[2:3], s[22:23], 2
	s_add_u32 s2, s62, s2
	s_addc_u32 s3, s63, s3
	s_load_dword s2, s[2:3], 0x0
	s_waitcnt lgkmcnt(0)
	s_lshl_b32 s2, s2, 2
	s_add_i32 s23, s2, s67

;     __device__ __forceinline__ bool next(int i, Unit& u) const {
;         int pl, n;
;         if (NT == 28 && G == 256 && l0 == 0) {
;             const int per = (nunits + 7) >> 3, x = c >> 5, j = c & 31, s = 32 * i + j; if (s >= per) return false;
;             const int L = x * per + s; if (L >= nunits) return false;
;             constexpr int PG = MOE_PG;
;             const int P = nunits / 28, full = (P / PG) * (PG * 28);
;             constexpr int NC = MOE_NC, NQ = 28 / NC;
;             if (L < full) { const int t = L / (NC * PG), r = L - t * (NC * PG), g = t / NQ, q = t - g * NQ; pl = PG * g + (r % PG); n = NC * q + (r / PG); }
;             else { const int L2 = L - full; pl = (P / PG) * PG + L2 / 28; n = L2 % 28; }
;         } else {
;         const int L = l0 + i * G + c; if (L >= nunits) return false;
;         pl = L / NT; n = L - pl * NT; }
;         const int p = p0 + pl;
;         const int e = __builtin_amdgcn_readfirstlane(pexp[p]);
;         u.pm = A_REL ? pl : p; u.po = A_REL ? p : pl; u.pn = n; u.pb = e * NT + n; return true;
.LBB0_1711:
	s_add_i32 s48, s48, 1
	s_mul_i32 s2, s48, s40
	s_add_i32 s2, s44, s2
	s_cmp_lt_i32 s2, s41
	s_cselect_b64 s[24:25], -1, 0
	s_cmp_ge_i32 s2, s41
	s_cbranch_scc1 .LBB0_1713
	s_ashr_i32 s3, s2, 31
	s_lshr_b32 s3, s3, 30
	s_add_i32 s3, s2, s3
	s_ashr_i32 s22, s3, 2
	s_and_b32 s3, s3, -4
	s_ashr_i32 s23, s22, 31
	s_sub_i32 s67, s2, s3
	s_lshl_b64 s[2:3], s[22:23], 2
	s_add_u32 s2, s62, s2
	s_addc_u32 s3, s63, s3
	s_load_dword s2, s[2:3], 0x0
	s_waitcnt lgkmcnt(0)
	s_lshl_b32 s2, s2, 2
	s_add_i32 s23, s2, s67
